# indexer scores as (w/2).d summed on the matrix cores via a combined bf16 query fragment plus one v_fma with |d| per head-score (relu(d)=(d+|d|)/2), scoring software-pipelined one head ahead
# speedup vs baseline: 1.0393x; 1.0038x over previous
.LBB0_1302:
	s_and_b64 s[14:15], s[28:29], exec
	s_cselect_b32 s14, s77, s76
	s_lshl_b32 s34, s14, 4
	s_mov_b32 s14, s33
	s_nop 0
	v_lshl_or_b32 v72, s14, 6, v195
	s_nop 0
	v_readfirstlane_b32 s14, v72
	s_ashr_i32 s30, s14, 6
	s_and_b32 s14, s34, 0xffffffc0
	s_add_i32 s14, s14, 64
	s_ashr_i32 s82, s14, 5
	v_and_b32_e32 v126, 63, v72
	v_and_b32_e32 v125, 15, v72
	s_cmpk_gt_i32 s14, 0x100
	s_mov_b64 s[14:15], -1
	s_cbranch_scc0 .LBB0_1545
	v_or_b32_e32 v0, s34, v125
	v_ashrrev_i32_e32 v1, 31, v0
	v_lshlrev_b64 v[2:3], 10, v[0:1]
	v_lshl_add_u64 v[2:3], s[26:27], 0, v[2:3]
	v_and_b32_e32 v176, 48, v126
	v_lshlrev_b64 v[0:1], 5, v[0:1]
	v_lshl_add_u64 v[68:69], v[2:3], 0, v[176:177]
	v_lshl_add_u64 v[12:13], s[24:25], 0, v[0:1]
	global_load_dwordx4 v[0:3], v[68:69], off
	global_load_dwordx4 v[4:7], v[68:69], off offset:64
	global_load_dwordx4 v[8:11], v[12:13], off offset:16
	s_nop 0
	global_load_dwordx4 v[12:15], v[12:13], off
	s_nop 0
	global_load_dwordx4 v[16:19], v[68:69], off offset:128
	global_load_dwordx4 v[20:23], v[68:69], off offset:192
	global_load_dwordx4 v[24:27], v[68:69], off offset:256
	global_load_dwordx4 v[28:31], v[68:69], off offset:320
	global_load_dwordx4 v[32:35], v[68:69], off offset:384
	global_load_dwordx4 v[36:39], v[68:69], off offset:448
	global_load_dwordx4 v[40:43], v[68:69], off offset:512
	global_load_dwordx4 v[44:47], v[68:69], off offset:576
	global_load_dwordx4 v[48:51], v[68:69], off offset:640
	global_load_dwordx4 v[52:55], v[68:69], off offset:704
	global_load_dwordx4 v[56:59], v[68:69], off offset:768
	global_load_dwordx4 v[60:63], v[68:69], off offset:832
	global_load_dwordx4 v[64:67], v[68:69], off offset:896
	s_nop 0
	global_load_dwordx4 v[68:71], v[68:69], off offset:960
	s_mov_b32 s74, s73
	s_mov_b32 s75, s73
	v_lshlrev_b32_e32 v73, 4, v72
	s_mov_b32 s72, s73
	v_mov_b64_e32 v[76:77], s[74:75]
	v_add_u32_e32 v122, 0, v73
	v_mov_b64_e32 v[74:75], s[72:73]
	v_cmp_gt_i32_e32 vcc, 17, v72
	s_waitcnt vmcnt(0)
	v_mul_f32_e32 v8, 0.5, v8
	v_mul_f32_e32 v9, 0.5, v9
	v_mul_f32_e32 v10, 0.5, v10
	v_mul_f32_e32 v11, 0.5, v11
	v_mul_f32_e32 v12, 0.5, v12
	v_mul_f32_e32 v13, 0.5, v13
	v_mul_f32_e32 v14, 0.5, v14
	v_mul_f32_e32 v15, 0.5, v15
	v_lshlrev_b32_e32 v155, 16, v0
	v_and_b32_e32 v168, 0xffff0000, v0
	v_mul_f32_e32 v169, v12, v155
	v_mul_f32_e32 v170, v12, v168
	v_lshlrev_b32_e32 v155, 16, v16
	v_and_b32_e32 v168, 0xffff0000, v16
	v_fmac_f32_e32 v169, v13, v155
	v_fmac_f32_e32 v170, v13, v168
	v_lshlrev_b32_e32 v155, 16, v24
	v_and_b32_e32 v168, 0xffff0000, v24
	v_fmac_f32_e32 v169, v14, v155
	v_fmac_f32_e32 v170, v14, v168
	v_lshlrev_b32_e32 v155, 16, v32
	v_and_b32_e32 v168, 0xffff0000, v32
	v_fmac_f32_e32 v169, v15, v155
	v_fmac_f32_e32 v170, v15, v168
	v_lshlrev_b32_e32 v155, 16, v40
	v_and_b32_e32 v168, 0xffff0000, v40
	v_fmac_f32_e32 v169, v8, v155
	v_fmac_f32_e32 v170, v8, v168
	v_lshlrev_b32_e32 v155, 16, v48
	v_and_b32_e32 v168, 0xffff0000, v48
	v_fmac_f32_e32 v169, v9, v155
	v_fmac_f32_e32 v170, v9, v168
	v_lshlrev_b32_e32 v155, 16, v56
	v_and_b32_e32 v168, 0xffff0000, v56
	v_fmac_f32_e32 v169, v10, v155
	v_fmac_f32_e32 v170, v10, v168
	v_lshlrev_b32_e32 v155, 16, v64
	v_and_b32_e32 v168, 0xffff0000, v64
	v_fmac_f32_e32 v169, v11, v155
	v_fmac_f32_e32 v170, v11, v168
	v_cvt_pk_bf16_f32 v244, v169, v170
	v_lshlrev_b32_e32 v155, 16, v1
	v_and_b32_e32 v168, 0xffff0000, v1
	v_mul_f32_e32 v169, v12, v155
	v_mul_f32_e32 v170, v12, v168
	v_lshlrev_b32_e32 v155, 16, v17
	v_and_b32_e32 v168, 0xffff0000, v17
	v_fmac_f32_e32 v169, v13, v155
	v_fmac_f32_e32 v170, v13, v168
	v_lshlrev_b32_e32 v155, 16, v25
	v_and_b32_e32 v168, 0xffff0000, v25
	v_fmac_f32_e32 v169, v14, v155
	v_fmac_f32_e32 v170, v14, v168
	v_lshlrev_b32_e32 v155, 16, v33
	v_and_b32_e32 v168, 0xffff0000, v33
	v_fmac_f32_e32 v169, v15, v155
	v_fmac_f32_e32 v170, v15, v168
	v_lshlrev_b32_e32 v155, 16, v41
	v_and_b32_e32 v168, 0xffff0000, v41
	v_fmac_f32_e32 v169, v8, v155
	v_fmac_f32_e32 v170, v8, v168
	v_lshlrev_b32_e32 v155, 16, v49
	v_and_b32_e32 v168, 0xffff0000, v49
	v_fmac_f32_e32 v169, v9, v155
	v_fmac_f32_e32 v170, v9, v168
	v_lshlrev_b32_e32 v155, 16, v57
	v_and_b32_e32 v168, 0xffff0000, v57
	v_fmac_f32_e32 v169, v10, v155
	v_fmac_f32_e32 v170, v10, v168
	v_lshlrev_b32_e32 v155, 16, v65
	v_and_b32_e32 v168, 0xffff0000, v65
	v_fmac_f32_e32 v169, v11, v155
	v_fmac_f32_e32 v170, v11, v168
	v_cvt_pk_bf16_f32 v245, v169, v170
	v_lshlrev_b32_e32 v155, 16, v2
	v_and_b32_e32 v168, 0xffff0000, v2
	v_mul_f32_e32 v169, v12, v155
	v_mul_f32_e32 v170, v12, v168
	v_lshlrev_b32_e32 v155, 16, v18
	v_and_b32_e32 v168, 0xffff0000, v18
	v_fmac_f32_e32 v169, v13, v155
	v_fmac_f32_e32 v170, v13, v168
	v_lshlrev_b32_e32 v155, 16, v26
	v_and_b32_e32 v168, 0xffff0000, v26
	v_fmac_f32_e32 v169, v14, v155
	v_fmac_f32_e32 v170, v14, v168
	v_lshlrev_b32_e32 v155, 16, v34
	v_and_b32_e32 v168, 0xffff0000, v34
	v_fmac_f32_e32 v169, v15, v155
	v_fmac_f32_e32 v170, v15, v168
	v_lshlrev_b32_e32 v155, 16, v42
	v_and_b32_e32 v168, 0xffff0000, v42
	v_fmac_f32_e32 v169, v8, v155
	v_fmac_f32_e32 v170, v8, v168
	v_lshlrev_b32_e32 v155, 16, v50
	v_and_b32_e32 v168, 0xffff0000, v50
	v_fmac_f32_e32 v169, v9, v155
	v_fmac_f32_e32 v170, v9, v168
	v_lshlrev_b32_e32 v155, 16, v58
	v_and_b32_e32 v168, 0xffff0000, v58
	v_fmac_f32_e32 v169, v10, v155
	v_fmac_f32_e32 v170, v10, v168
	v_lshlrev_b32_e32 v155, 16, v66
	v_and_b32_e32 v168, 0xffff0000, v66
	v_fmac_f32_e32 v169, v11, v155
	v_fmac_f32_e32 v170, v11, v168
	v_cvt_pk_bf16_f32 v246, v169, v170
	v_lshlrev_b32_e32 v155, 16, v3
	v_and_b32_e32 v168, 0xffff0000, v3
	v_mul_f32_e32 v169, v12, v155
	v_mul_f32_e32 v170, v12, v168
	v_lshlrev_b32_e32 v155, 16, v19
	v_and_b32_e32 v168, 0xffff0000, v19
	v_fmac_f32_e32 v169, v13, v155
	v_fmac_f32_e32 v170, v13, v168
	v_lshlrev_b32_e32 v155, 16, v27
	v_and_b32_e32 v168, 0xffff0000, v27
	v_fmac_f32_e32 v169, v14, v155
	v_fmac_f32_e32 v170, v14, v168
	v_lshlrev_b32_e32 v155, 16, v35
	v_and_b32_e32 v168, 0xffff0000, v35
	v_fmac_f32_e32 v169, v15, v155
	v_fmac_f32_e32 v170, v15, v168
	v_lshlrev_b32_e32 v155, 16, v43
	v_and_b32_e32 v168, 0xffff0000, v43
	v_fmac_f32_e32 v169, v8, v155
	v_fmac_f32_e32 v170, v8, v168
	v_lshlrev_b32_e32 v155, 16, v51
	v_and_b32_e32 v168, 0xffff0000, v51
	v_fmac_f32_e32 v169, v9, v155
	v_fmac_f32_e32 v170, v9, v168
	v_lshlrev_b32_e32 v155, 16, v59
	v_and_b32_e32 v168, 0xffff0000, v59
	v_fmac_f32_e32 v169, v10, v155
	v_fmac_f32_e32 v170, v10, v168
	v_lshlrev_b32_e32 v155, 16, v67
	v_and_b32_e32 v168, 0xffff0000, v67
	v_fmac_f32_e32 v169, v11, v155
	v_fmac_f32_e32 v170, v11, v168
	v_cvt_pk_bf16_f32 v247, v169, v170
	v_lshlrev_b32_e32 v155, 16, v4
	v_and_b32_e32 v168, 0xffff0000, v4
	v_mul_f32_e32 v169, v12, v155
	v_mul_f32_e32 v170, v12, v168
	v_lshlrev_b32_e32 v155, 16, v20
	v_and_b32_e32 v168, 0xffff0000, v20
	v_fmac_f32_e32 v169, v13, v155
	v_fmac_f32_e32 v170, v13, v168
	v_lshlrev_b32_e32 v155, 16, v28
	v_and_b32_e32 v168, 0xffff0000, v28
	v_fmac_f32_e32 v169, v14, v155
	v_fmac_f32_e32 v170, v14, v168
	v_lshlrev_b32_e32 v155, 16, v36
	v_and_b32_e32 v168, 0xffff0000, v36
	v_fmac_f32_e32 v169, v15, v155
	v_fmac_f32_e32 v170, v15, v168
	v_lshlrev_b32_e32 v155, 16, v44
	v_and_b32_e32 v168, 0xffff0000, v44
	v_fmac_f32_e32 v169, v8, v155
	v_fmac_f32_e32 v170, v8, v168
	v_lshlrev_b32_e32 v155, 16, v52
	v_and_b32_e32 v168, 0xffff0000, v52
	v_fmac_f32_e32 v169, v9, v155
	v_fmac_f32_e32 v170, v9, v168
	v_lshlrev_b32_e32 v155, 16, v60
	v_and_b32_e32 v168, 0xffff0000, v60
	v_fmac_f32_e32 v169, v10, v155
	v_fmac_f32_e32 v170, v10, v168
	v_lshlrev_b32_e32 v155, 16, v68
	v_and_b32_e32 v168, 0xffff0000, v68
	v_fmac_f32_e32 v169, v11, v155
	v_fmac_f32_e32 v170, v11, v168
	v_cvt_pk_bf16_f32 v248, v169, v170
	v_lshlrev_b32_e32 v155, 16, v5
	v_and_b32_e32 v168, 0xffff0000, v5
	v_mul_f32_e32 v169, v12, v155
	v_mul_f32_e32 v170, v12, v168
	v_lshlrev_b32_e32 v155, 16, v21
	v_and_b32_e32 v168, 0xffff0000, v21
	v_fmac_f32_e32 v169, v13, v155
	v_fmac_f32_e32 v170, v13, v168
	v_lshlrev_b32_e32 v155, 16, v29
	v_and_b32_e32 v168, 0xffff0000, v29
	v_fmac_f32_e32 v169, v14, v155
	v_fmac_f32_e32 v170, v14, v168
	v_lshlrev_b32_e32 v155, 16, v37
	v_and_b32_e32 v168, 0xffff0000, v37
	v_fmac_f32_e32 v169, v15, v155
	v_fmac_f32_e32 v170, v15, v168
	v_lshlrev_b32_e32 v155, 16, v45
	v_and_b32_e32 v168, 0xffff0000, v45
	v_fmac_f32_e32 v169, v8, v155
	v_fmac_f32_e32 v170, v8, v168
	v_lshlrev_b32_e32 v155, 16, v53
	v_and_b32_e32 v168, 0xffff0000, v53
	v_fmac_f32_e32 v169, v9, v155
	v_fmac_f32_e32 v170, v9, v168
	v_lshlrev_b32_e32 v155, 16, v61
	v_and_b32_e32 v168, 0xffff0000, v61
	v_fmac_f32_e32 v169, v10, v155
	v_fmac_f32_e32 v170, v10, v168
	v_lshlrev_b32_e32 v155, 16, v69
	v_and_b32_e32 v168, 0xffff0000, v69
	v_fmac_f32_e32 v169, v11, v155
	v_fmac_f32_e32 v170, v11, v168
	v_cvt_pk_bf16_f32 v249, v169, v170
	v_lshlrev_b32_e32 v155, 16, v6
	v_and_b32_e32 v168, 0xffff0000, v6
	v_mul_f32_e32 v169, v12, v155
	v_mul_f32_e32 v170, v12, v168
	v_lshlrev_b32_e32 v155, 16, v22
	v_and_b32_e32 v168, 0xffff0000, v22
	v_fmac_f32_e32 v169, v13, v155
	v_fmac_f32_e32 v170, v13, v168
	v_lshlrev_b32_e32 v155, 16, v30
	v_and_b32_e32 v168, 0xffff0000, v30
	v_fmac_f32_e32 v169, v14, v155
	v_fmac_f32_e32 v170, v14, v168
	v_lshlrev_b32_e32 v155, 16, v38
	v_and_b32_e32 v168, 0xffff0000, v38
	v_fmac_f32_e32 v169, v15, v155
	v_fmac_f32_e32 v170, v15, v168
	v_lshlrev_b32_e32 v155, 16, v46
	v_and_b32_e32 v168, 0xffff0000, v46
	v_fmac_f32_e32 v169, v8, v155
	v_fmac_f32_e32 v170, v8, v168
	v_lshlrev_b32_e32 v155, 16, v54
	v_and_b32_e32 v168, 0xffff0000, v54
	v_fmac_f32_e32 v169, v9, v155
	v_fmac_f32_e32 v170, v9, v168
	v_lshlrev_b32_e32 v155, 16, v62
	v_and_b32_e32 v168, 0xffff0000, v62
	v_fmac_f32_e32 v169, v10, v155
	v_fmac_f32_e32 v170, v10, v168
	v_lshlrev_b32_e32 v155, 16, v70
	v_and_b32_e32 v168, 0xffff0000, v70
	v_fmac_f32_e32 v169, v11, v155
	v_fmac_f32_e32 v170, v11, v168
	v_cvt_pk_bf16_f32 v250, v169, v170
	v_lshlrev_b32_e32 v155, 16, v7
	v_and_b32_e32 v168, 0xffff0000, v7
	v_mul_f32_e32 v169, v12, v155
	v_mul_f32_e32 v170, v12, v168
	v_lshlrev_b32_e32 v155, 16, v23
	v_and_b32_e32 v168, 0xffff0000, v23
	v_fmac_f32_e32 v169, v13, v155
	v_fmac_f32_e32 v170, v13, v168
	v_lshlrev_b32_e32 v155, 16, v31
	v_and_b32_e32 v168, 0xffff0000, v31
	v_fmac_f32_e32 v169, v14, v155
	v_fmac_f32_e32 v170, v14, v168
	v_lshlrev_b32_e32 v155, 16, v39
	v_and_b32_e32 v168, 0xffff0000, v39
	v_fmac_f32_e32 v169, v15, v155
	v_fmac_f32_e32 v170, v15, v168
	v_lshlrev_b32_e32 v155, 16, v47
	v_and_b32_e32 v168, 0xffff0000, v47
	v_fmac_f32_e32 v169, v8, v155
	v_fmac_f32_e32 v170, v8, v168
	v_lshlrev_b32_e32 v155, 16, v55
	v_and_b32_e32 v168, 0xffff0000, v55
	v_fmac_f32_e32 v169, v9, v155
	v_fmac_f32_e32 v170, v9, v168
	v_lshlrev_b32_e32 v155, 16, v63
	v_and_b32_e32 v168, 0xffff0000, v63
	v_fmac_f32_e32 v169, v10, v155
	v_fmac_f32_e32 v170, v10, v168
	v_lshlrev_b32_e32 v155, 16, v71
	v_and_b32_e32 v168, 0xffff0000, v71
	v_fmac_f32_e32 v169, v11, v155
	v_fmac_f32_e32 v170, v11, v168
	v_cvt_pk_bf16_f32 v251, v169, v170
	s_barrier
	ds_write_b128 v122, v[74:77]
	ds_write_b128 v122, v[74:77] offset:8192
	ds_write_b128 v122, v[74:77] offset:16384
	ds_write_b128 v122, v[74:77] offset:24576
	ds_write_b128 v122, v[74:77] offset:32768
	ds_write_b128 v122, v[74:77] offset:40960
	ds_write_b128 v122, v[74:77] offset:49152
	ds_write_b128 v122, v[74:77] offset:57344
	s_and_saveexec_b64 s[14:15], vcc
	v_lshl_add_u32 v72, v72, 2, s3
	ds_write_b32 v72, v177 offset:192
	s_or_b64 exec, exec, s[14:15]
	s_lshl_b32 s83, s30, 5
	v_or_b32_e32 v72, s83, v125
	v_lshrrev_b32_e32 v127, 4, v126
	v_ashrrev_i32_e32 v73, 31, v72
	v_lshlrev_b32_e32 v74, 3, v127
	v_mul_u32_u24_e32 v229, 0x70, v125
	v_lshlrev_b64 v[72:73], 7, v[72:73]
	v_sub_u32_e32 v72, v72, v229
	v_lshl_add_u64 v[72:73], s[22:23], 0, v[72:73]
	v_lshlrev_b32_e32 v176, 5, v74
	v_lshl_add_u64 v[72:73], v[72:73], 0, v[176:177]
	s_waitcnt lgkmcnt(0)
	s_barrier
	global_load_dwordx4 v[100:103], v[72:73], off
	global_load_dwordx4 v[96:99], v[72:73], off offset:1024
	global_load_dwordx4 v[92:95], v[72:73], off offset:2048
	global_load_dwordx4 v[88:91], v[72:73], off offset:3072
	s_cmp_lt_i32 s30, s82
	v_lshl_add_u32 v128, v125, 12, 0
	s_cselect_b64 s[36:37], -1, 0
	s_cmp_ge_i32 s30, s82
	v_lshl_add_u64 v[120:121], s[22:23], 0, v[176:177]
	s_cbranch_scc1 .LBB0_1310
	s_waitcnt vmcnt(0)
	v_mov_b64_e32 v[106:107], v[90:91]
	s_add_i32 s14, s82, -1
	s_mov_b32 s15, s30
	v_mov_b64_e32 v[104:105], v[88:89]
	v_mov_b32_e32 v116, v100
	v_mov_b32_e32 v117, v101
	v_mov_b32_e32 v118, v102
	v_mov_b32_e32 v119, v103
	v_mov_b32_e32 v108, v96
	v_mov_b32_e32 v109, v97
	v_mov_b32_e32 v110, v98
	v_mov_b32_e32 v111, v99
	v_mov_b32_e32 v112, v92
	v_mov_b32_e32 v113, v93
	v_mov_b32_e32 v114, v94
	v_mov_b32_e32 v115, v95
	v_lshl_add_u32 v232, s100, 11, v230
	s_branch .LBB0_1308

.LBB0_1308:
	s_waitcnt vmcnt(5)
	v_mfma_f32_16x16x32_bf16 v[130:133], v[116:119], v[0:3], 0
	v_mfma_f32_16x16x32_bf16 v[156:159], v[116:119], v[244:247], 0
	s_min_i32 s32, s15, s100
	v_lshl_add_u32 v231, s32, 11, v230
	s_add_i32 s31, s15, 8
	s_min_i32 s35, s31, s14
	v_lshl_or_b32 v72, s35, 5, v125
	s_waitcnt vmcnt(3)
	v_mfma_f32_16x16x32_bf16 v[134:137], v[112:115], v[0:3], 0
	v_mfma_f32_16x16x32_bf16 v[160:163], v[112:115], v[244:247], 0
	v_ashrrev_i32_e32 v73, 31, v72
	v_lshlrev_b64 v[72:73], 7, v[72:73]
	v_sub_u32_e32 v72, v72, v229
	v_lshl_add_u64 v[84:85], v[120:121], 0, v[72:73]
	v_mfma_f32_16x16x32_bf16 v[138:141], v[108:111], v[4:7], v[130:133]
	v_mfma_f32_16x16x32_bf16 v[156:159], v[108:111], v[248:251], v[156:159]
	global_load_dwordx4 v[72:75], v[84:85], off
	global_load_dwordx4 v[76:79], v[84:85], off offset:1024
	global_load_dwordx4 v[80:83], v[84:85], off offset:2048
	s_nop 0
	global_load_dwordx4 v[84:87], v[84:85], off offset:3072
	global_store_dwordx4 v232, v[164:167], s[20:21]
	global_store_dwordx4 v232, v[186:189], s[20:21] offset:1024
	s_nop 1
	s_nop 0
	s_add_i32 s15, s15, 16
	s_waitcnt vmcnt(8)
	v_mfma_f32_16x16x32_bf16 v[132:135], v[104:107], v[4:7], v[134:137]
	v_mfma_f32_16x16x32_bf16 v[160:163], v[104:107], v[248:251], v[160:163]
	s_min_i32 s35, s15, s14
	s_cmp_ge_i32 s31, s82
	v_mfma_f32_16x16x32_bf16 v[142:145], v[116:119], v[16:19], 0
	v_mfma_f32_16x16x32_bf16 v[146:149], v[112:115], v[16:19], 0
	v_mfma_f32_16x16x32_bf16 v[142:145], v[108:111], v[20:23], v[142:145]
	v_mfma_f32_16x16x32_bf16 v[146:149], v[104:107], v[20:23], v[146:149]
	s_nop 3
	v_fma_f32 v156, v12, |v138|, v156
	v_fma_f32 v160, v12, |v132|, v160
	v_fma_f32 v157, v12, |v139|, v157
	v_fma_f32 v161, v12, |v133|, v161
	v_fma_f32 v158, v12, |v140|, v158
	v_fma_f32 v162, v12, |v134|, v162
	v_fma_f32 v159, v12, |v141|, v159
	v_fma_f32 v163, v12, |v135|, v163
	v_mfma_f32_16x16x32_bf16 v[138:141], v[116:119], v[24:27], 0
	v_mfma_f32_16x16x32_bf16 v[132:135], v[112:115], v[24:27], 0
	v_mfma_f32_16x16x32_bf16 v[138:141], v[108:111], v[28:31], v[138:141]
	v_mfma_f32_16x16x32_bf16 v[132:135], v[104:107], v[28:31], v[132:135]
	s_nop 3
	v_fma_f32 v156, v13, |v142|, v156
	v_fma_f32 v160, v13, |v146|, v160
	v_fma_f32 v157, v13, |v143|, v157
	v_fma_f32 v161, v13, |v147|, v161
	v_fma_f32 v158, v13, |v144|, v158
	v_fma_f32 v162, v13, |v148|, v162
	v_fma_f32 v159, v13, |v145|, v159
	v_fma_f32 v163, v13, |v149|, v163
	v_mfma_f32_16x16x32_bf16 v[142:145], v[116:119], v[32:35], 0
	v_mfma_f32_16x16x32_bf16 v[146:149], v[112:115], v[32:35], 0
	v_mfma_f32_16x16x32_bf16 v[142:145], v[108:111], v[36:39], v[142:145]
	v_mfma_f32_16x16x32_bf16 v[146:149], v[104:107], v[36:39], v[146:149]
	s_nop 3
	v_fma_f32 v156, v14, |v138|, v156
	v_fma_f32 v160, v14, |v132|, v160
	v_fma_f32 v157, v14, |v139|, v157
	v_fma_f32 v161, v14, |v133|, v161
	v_fma_f32 v158, v14, |v140|, v158
	v_fma_f32 v162, v14, |v134|, v162
	v_fma_f32 v159, v14, |v141|, v159
	v_fma_f32 v163, v14, |v135|, v163
	v_mfma_f32_16x16x32_bf16 v[138:141], v[116:119], v[40:43], 0
	v_mfma_f32_16x16x32_bf16 v[132:135], v[112:115], v[40:43], 0
	v_mfma_f32_16x16x32_bf16 v[138:141], v[108:111], v[44:47], v[138:141]
	v_mfma_f32_16x16x32_bf16 v[132:135], v[104:107], v[44:47], v[132:135]
	s_nop 3
	v_fma_f32 v156, v15, |v142|, v156
	v_fma_f32 v160, v15, |v146|, v160
	v_fma_f32 v157, v15, |v143|, v157
	v_fma_f32 v161, v15, |v147|, v161
	v_fma_f32 v158, v15, |v144|, v158
	v_fma_f32 v162, v15, |v148|, v162
	v_fma_f32 v159, v15, |v145|, v159
	v_fma_f32 v163, v15, |v149|, v163
	v_mfma_f32_16x16x32_bf16 v[142:145], v[116:119], v[48:51], 0
	v_mfma_f32_16x16x32_bf16 v[146:149], v[112:115], v[48:51], 0
	v_mfma_f32_16x16x32_bf16 v[142:145], v[108:111], v[52:55], v[142:145]
	v_mfma_f32_16x16x32_bf16 v[146:149], v[104:107], v[52:55], v[146:149]
	s_nop 3
	v_fma_f32 v156, v8, |v138|, v156
	v_fma_f32 v160, v8, |v132|, v160
	v_fma_f32 v157, v8, |v139|, v157
	v_fma_f32 v161, v8, |v133|, v161
	v_fma_f32 v158, v8, |v140|, v158
	v_fma_f32 v162, v8, |v134|, v162
	v_fma_f32 v159, v8, |v141|, v159
	v_fma_f32 v163, v8, |v135|, v163
	v_mfma_f32_16x16x32_bf16 v[138:141], v[116:119], v[56:59], 0
	v_mfma_f32_16x16x32_bf16 v[132:135], v[112:115], v[56:59], 0
	v_mfma_f32_16x16x32_bf16 v[138:141], v[108:111], v[60:63], v[138:141]
	v_mfma_f32_16x16x32_bf16 v[132:135], v[104:107], v[60:63], v[132:135]
	s_nop 3
	v_fma_f32 v156, v9, |v142|, v156
	v_fma_f32 v160, v9, |v146|, v160
	v_fma_f32 v157, v9, |v143|, v157
	v_fma_f32 v161, v9, |v147|, v161
	v_fma_f32 v158, v9, |v144|, v158
	v_fma_f32 v162, v9, |v148|, v162
	v_fma_f32 v159, v9, |v145|, v159
	v_fma_f32 v163, v9, |v149|, v163
	v_mfma_f32_16x16x32_bf16 v[142:145], v[116:119], v[64:67], 0
	v_mfma_f32_16x16x32_bf16 v[146:149], v[112:115], v[64:67], 0
	v_mfma_f32_16x16x32_bf16 v[142:145], v[108:111], v[68:71], v[142:145]
	v_mfma_f32_16x16x32_bf16 v[146:149], v[104:107], v[68:71], v[146:149]
	s_nop 3
	v_fma_f32 v156, v10, |v138|, v156
	v_fma_f32 v160, v10, |v132|, v160
	v_fma_f32 v157, v10, |v139|, v157
	v_fma_f32 v161, v10, |v133|, v161
	v_fma_f32 v158, v10, |v140|, v158
	v_fma_f32 v162, v10, |v134|, v162
	v_fma_f32 v159, v10, |v141|, v159
	v_fma_f32 v163, v10, |v135|, v163
	s_nop 7
	v_fma_f32 v156, v11, |v142|, v156
	v_fma_f32 v160, v11, |v146|, v160
	v_fma_f32 v157, v11, |v143|, v157
	v_fma_f32 v161, v11, |v147|, v161
	v_fma_f32 v158, v11, |v144|, v158
	v_fma_f32 v162, v11, |v148|, v162
	v_fma_f32 v159, v11, |v145|, v159
	v_fma_f32 v163, v11, |v149|, v163
	s_nop 0
	v_lshrrev_b32 v104, 22, v156
	v_bfe_u32 v105, v156, 21, 1
	v_lshl_add_u32 v104, v104, 2, v128
	v_mad_u32_u24 v105, v105, s1, 1
	ds_add_u32 v104, v105
	v_lshrrev_b32 v104, 22, v157
	v_bfe_u32 v105, v157, 21, 1
	v_lshl_add_u32 v104, v104, 2, v128
	v_mad_u32_u24 v105, v105, s1, 1
	ds_add_u32 v104, v105
	v_lshrrev_b32 v104, 22, v158
	v_bfe_u32 v105, v158, 21, 1
	v_lshl_add_u32 v104, v104, 2, v128
	v_mad_u32_u24 v105, v105, s1, 1
	ds_add_u32 v104, v105
	v_lshrrev_b32 v104, 22, v159
	v_bfe_u32 v105, v159, 21, 1
	v_lshl_add_u32 v104, v104, 2, v128
	v_mad_u32_u24 v105, v105, s1, 1
	ds_add_u32 v104, v105
	v_lshrrev_b32 v104, 22, v160
	v_bfe_u32 v105, v160, 21, 1
	v_lshl_add_u32 v104, v104, 2, v128
	v_mad_u32_u24 v105, v105, s1, 1
	ds_add_u32 v104, v105
	v_lshrrev_b32 v104, 22, v161
	v_bfe_u32 v105, v161, 21, 1
	v_lshl_add_u32 v104, v104, 2, v128
	v_mad_u32_u24 v105, v105, s1, 1
	ds_add_u32 v104, v105
	v_lshrrev_b32 v104, 22, v162
	v_bfe_u32 v105, v162, 21, 1
	v_lshl_add_u32 v104, v104, 2, v128
	v_mad_u32_u24 v105, v105, s1, 1
	ds_add_u32 v104, v105
	v_lshrrev_b32 v104, 22, v163
	v_bfe_u32 v105, v163, 21, 1
	v_lshl_add_u32 v104, v104, 2, v128
	v_mad_u32_u24 v105, v105, s1, 1
	ds_add_u32 v104, v105
	v_lshl_or_b32 v104, s35, 5, v125
	v_ashrrev_i32_e32 v105, 31, v104
	v_lshlrev_b64 v[104:105], 7, v[104:105]
	v_sub_u32_e32 v104, v104, v229
	v_lshl_add_u64 v[104:105], v[120:121], 0, v[104:105]
	global_load_dwordx4 v[116:119], v[104:105], off
	global_load_dwordx4 v[108:111], v[104:105], off offset:1024
	global_load_dwordx4 v[112:115], v[104:105], off offset:2048
	s_nop 0
	global_load_dwordx4 v[104:107], v[104:105], off offset:3072
	global_store_dwordx4 v231, v[156:159], s[20:21]
	global_store_dwordx4 v231, v[160:163], s[20:21] offset:1024
	s_cbranch_scc1 .LBB0_1307
	s_waitcnt vmcnt(11)
	v_mfma_f32_16x16x32_bf16 v[130:133], v[72:75], v[0:3], 0
	v_mfma_f32_16x16x32_bf16 v[164:167], v[72:75], v[244:247], 0
	s_min_i32 s32, s31, s100
	v_lshl_add_u32 v232, s32, 11, v230
	s_waitcnt vmcnt(9)
	v_mfma_f32_16x16x32_bf16 v[134:137], v[80:83], v[0:3], 0
	v_mfma_f32_16x16x32_bf16 v[186:189], v[80:83], v[244:247], 0
	v_mfma_f32_16x16x32_bf16 v[138:141], v[76:79], v[4:7], v[130:133]
	v_mfma_f32_16x16x32_bf16 v[164:167], v[76:79], v[248:251], v[164:167]
	s_waitcnt vmcnt(8)
	v_mfma_f32_16x16x32_bf16 v[132:135], v[84:87], v[4:7], v[134:137]
	v_mfma_f32_16x16x32_bf16 v[186:189], v[84:87], v[248:251], v[186:189]
	v_mfma_f32_16x16x32_bf16 v[142:145], v[72:75], v[16:19], 0
	v_mfma_f32_16x16x32_bf16 v[146:149], v[80:83], v[16:19], 0
	v_mfma_f32_16x16x32_bf16 v[142:145], v[76:79], v[20:23], v[142:145]
	v_mfma_f32_16x16x32_bf16 v[146:149], v[84:87], v[20:23], v[146:149]
	s_nop 3
	v_fma_f32 v164, v12, |v138|, v164
	v_fma_f32 v186, v12, |v132|, v186
	v_fma_f32 v165, v12, |v139|, v165
	v_fma_f32 v187, v12, |v133|, v187
	v_fma_f32 v166, v12, |v140|, v166
	v_fma_f32 v188, v12, |v134|, v188
	v_fma_f32 v167, v12, |v141|, v167
	v_fma_f32 v189, v12, |v135|, v189
	v_mfma_f32_16x16x32_bf16 v[138:141], v[72:75], v[24:27], 0
	v_mfma_f32_16x16x32_bf16 v[132:135], v[80:83], v[24:27], 0
	v_mfma_f32_16x16x32_bf16 v[138:141], v[76:79], v[28:31], v[138:141]
	v_mfma_f32_16x16x32_bf16 v[132:135], v[84:87], v[28:31], v[132:135]
	s_nop 3
	v_fma_f32 v164, v13, |v142|, v164
	v_fma_f32 v186, v13, |v146|, v186
	v_fma_f32 v165, v13, |v143|, v165
	v_fma_f32 v187, v13, |v147|, v187
	v_fma_f32 v166, v13, |v144|, v166
	v_fma_f32 v188, v13, |v148|, v188
	v_fma_f32 v167, v13, |v145|, v167
	v_fma_f32 v189, v13, |v149|, v189
	v_mfma_f32_16x16x32_bf16 v[142:145], v[72:75], v[32:35], 0
	v_mfma_f32_16x16x32_bf16 v[146:149], v[80:83], v[32:35], 0
	v_mfma_f32_16x16x32_bf16 v[142:145], v[76:79], v[36:39], v[142:145]
	v_mfma_f32_16x16x32_bf16 v[146:149], v[84:87], v[36:39], v[146:149]
	s_nop 3
	v_fma_f32 v164, v14, |v138|, v164
	v_fma_f32 v186, v14, |v132|, v186
	v_fma_f32 v165, v14, |v139|, v165
	v_fma_f32 v187, v14, |v133|, v187
	v_fma_f32 v166, v14, |v140|, v166
	v_fma_f32 v188, v14, |v134|, v188
	v_fma_f32 v167, v14, |v141|, v167
	v_fma_f32 v189, v14, |v135|, v189
	v_mfma_f32_16x16x32_bf16 v[138:141], v[72:75], v[40:43], 0
	v_mfma_f32_16x16x32_bf16 v[132:135], v[80:83], v[40:43], 0
	v_mfma_f32_16x16x32_bf16 v[138:141], v[76:79], v[44:47], v[138:141]
	v_mfma_f32_16x16x32_bf16 v[132:135], v[84:87], v[44:47], v[132:135]
	s_nop 3
	v_fma_f32 v164, v15, |v142|, v164
	v_fma_f32 v186, v15, |v146|, v186
	v_fma_f32 v165, v15, |v143|, v165
	v_fma_f32 v187, v15, |v147|, v187
	v_fma_f32 v166, v15, |v144|, v166
	v_fma_f32 v188, v15, |v148|, v188
	v_fma_f32 v167, v15, |v145|, v167
	v_fma_f32 v189, v15, |v149|, v189
	v_mfma_f32_16x16x32_bf16 v[142:145], v[72:75], v[48:51], 0
	v_mfma_f32_16x16x32_bf16 v[146:149], v[80:83], v[48:51], 0
	v_mfma_f32_16x16x32_bf16 v[142:145], v[76:79], v[52:55], v[142:145]
	v_mfma_f32_16x16x32_bf16 v[146:149], v[84:87], v[52:55], v[146:149]
	s_nop 3
	v_fma_f32 v164, v8, |v138|, v164
	v_fma_f32 v186, v8, |v132|, v186
	v_fma_f32 v165, v8, |v139|, v165
	v_fma_f32 v187, v8, |v133|, v187
	v_fma_f32 v166, v8, |v140|, v166
	v_fma_f32 v188, v8, |v134|, v188
	v_fma_f32 v167, v8, |v141|, v167
	v_fma_f32 v189, v8, |v135|, v189
	v_mfma_f32_16x16x32_bf16 v[138:141], v[72:75], v[56:59], 0
	v_mfma_f32_16x16x32_bf16 v[132:135], v[80:83], v[56:59], 0
	v_mfma_f32_16x16x32_bf16 v[138:141], v[76:79], v[60:63], v[138:141]
	v_mfma_f32_16x16x32_bf16 v[132:135], v[84:87], v[60:63], v[132:135]
	s_nop 3
	v_fma_f32 v164, v9, |v142|, v164
	v_fma_f32 v186, v9, |v146|, v186
	v_fma_f32 v165, v9, |v143|, v165
	v_fma_f32 v187, v9, |v147|, v187
	v_fma_f32 v166, v9, |v144|, v166
	v_fma_f32 v188, v9, |v148|, v188
	v_fma_f32 v167, v9, |v145|, v167
	v_fma_f32 v189, v9, |v149|, v189
	v_mfma_f32_16x16x32_bf16 v[142:145], v[72:75], v[64:67], 0
	v_mfma_f32_16x16x32_bf16 v[146:149], v[80:83], v[64:67], 0
	v_mfma_f32_16x16x32_bf16 v[142:145], v[76:79], v[68:71], v[142:145]
	v_mfma_f32_16x16x32_bf16 v[146:149], v[84:87], v[68:71], v[146:149]
	s_nop 3
	v_fma_f32 v164, v10, |v138|, v164
	v_fma_f32 v186, v10, |v132|, v186
	v_fma_f32 v165, v10, |v139|, v165
	v_fma_f32 v187, v10, |v133|, v187
	v_fma_f32 v166, v10, |v140|, v166
	v_fma_f32 v188, v10, |v134|, v188
	v_fma_f32 v167, v10, |v141|, v167
	v_fma_f32 v189, v10, |v135|, v189
	s_nop 7
	v_fma_f32 v164, v11, |v142|, v164
	v_fma_f32 v186, v11, |v146|, v186
	v_fma_f32 v165, v11, |v143|, v165
	v_fma_f32 v187, v11, |v147|, v187
	v_fma_f32 v166, v11, |v144|, v166
	v_fma_f32 v188, v11, |v148|, v188
	v_fma_f32 v167, v11, |v145|, v167
	v_fma_f32 v189, v11, |v149|, v189
	v_lshrrev_b32 v135, 22, v164
	v_bfe_u32 v131, v164, 21, 1
	v_mad_u32_u24 v131, v131, s1, 1
	v_lshl_add_u32 v135, v135, 2, v128
	ds_add_u32 v135, v131
	v_lshrrev_b32 v131, 22, v165
	v_bfe_u32 v132, v165, 21, 1
	v_lshl_add_u32 v131, v131, 2, v128
	v_mad_u32_u24 v132, v132, s1, 1
	ds_add_u32 v131, v132
	v_lshrrev_b32 v131, 22, v166
	v_bfe_u32 v132, v166, 21, 1
	v_lshl_add_u32 v131, v131, 2, v128
	v_mad_u32_u24 v132, v132, s1, 1
	ds_add_u32 v131, v132
	v_lshrrev_b32 v131, 22, v167
	v_bfe_u32 v132, v167, 21, 1
	v_lshl_add_u32 v131, v131, 2, v128
	v_mad_u32_u24 v132, v132, s1, 1
	ds_add_u32 v131, v132
	v_lshrrev_b32 v131, 22, v186
	v_bfe_u32 v123, v186, 21, 1
	v_mad_u32_u24 v123, v123, s1, 1
	v_lshl_add_u32 v131, v131, 2, v128
	ds_add_u32 v131, v123
	v_lshrrev_b32 v123, 22, v187
	v_bfe_u32 v124, v187, 21, 1
	v_lshl_add_u32 v123, v123, 2, v128
	v_mad_u32_u24 v124, v124, s1, 1
	ds_add_u32 v123, v124
	v_lshrrev_b32 v123, 22, v188
	v_bfe_u32 v124, v188, 21, 1
	v_lshl_add_u32 v123, v123, 2, v128
	v_mad_u32_u24 v124, v124, s1, 1
	ds_add_u32 v123, v124
	v_lshrrev_b32 v123, 22, v189
	v_bfe_u32 v124, v189, 21, 1
	v_lshl_add_u32 v123, v123, 2, v128
	v_mad_u32_u24 v124, v124, s1, 1
	ds_add_u32 v123, v124
	s_cmp_ge_i32 s15, s82
	s_cbranch_scc0 .LBB0_1308
	global_store_dwordx4 v232, v[164:167], s[20:21]
	global_store_dwordx4 v232, v[186:189], s[20:21] offset:1024
	s_branch .LBB0_1310

.Lpb2_entry:
	s_waitcnt vmcnt(0)
	s_min_i32 s32, s82, s100
	v_mov_b32_e32 v235, 0xffff
	v_ashrrev_i32_e32 v196, 31, v139
	v_lshl_add_u32 v234, s100, 11, v230
	v_lshl_add_u32 v233, s31, 11, v230
	global_load_dwordx4 v[156:159], v233, s[20:21]
	global_load_dwordx4 v[160:163], v233, s[20:21] offset:1024
	global_store_dword v234, v193, s[20:21]
	s_add_i32 s85, s31, 8
	s_min_i32 s85, s85, s100
	v_lshl_add_u32 v233, s85, 11, v230
	global_load_dwordx4 v[178:181], v233, s[20:21]
	global_load_dwordx4 v[182:185], v233, s[20:21] offset:1024
	global_store_dword v234, v193, s[20:21]
	s_add_i32 s85, s31, 16
	s_min_i32 s85, s85, s100
	v_lshl_add_u32 v233, s85, 11, v230
	global_load_dwordx4 v[236:239], v233, s[20:21]
	global_load_dwordx4 v[240:243], v233, s[20:21] offset:1024
	global_store_dword v234, v193, s[20:21]
	s_add_i32 s85, s31, 24
	s_min_i32 s85, s85, s100
	v_lshl_add_u32 v233, s85, 11, v230
	global_load_dwordx4 v[80:83], v233, s[20:21]
	global_load_dwordx4 v[84:87], v233, s[20:21] offset:1024
	global_store_dword v234, v193, s[20:21]
.Lpb2_i0:
	s_add_i32 s85, s31, 32
	s_min_i32 s85, s85, s100
	v_lshl_add_u32 v233, s85, 11, v230
	global_load_dwordx4 v[72:75], v233, s[20:21]
	global_load_dwordx4 v[76:79], v233, s[20:21] offset:1024
	s_waitcnt vmcnt(12)
	v_cmp_ge_f32_e64 s[66:67], v156, v140
	v_cmp_ge_f32_e64 s[50:51], v156, v139
	v_cmp_ge_f32_e32 vcc, v157, v140
	v_cmp_ge_f32_e64 s[52:53], v157, v139
	v_cndmask_b32_e64 v224, 0, 1, s[66:67]
	v_cndmask_b32_e64 v225, 0, 2, vcc
	s_andn2_b64 s[50:51], s[50:51], s[66:67]
	s_andn2_b64 s[52:53], s[52:53], vcc
	v_or_b32_e32 v228, v224, v225
	v_cmp_ge_f32_e64 s[66:67], v158, v140
	v_cmp_ge_f32_e64 s[54:55], v158, v139
	v_cmp_ge_f32_e32 vcc, v159, v140
	v_cmp_ge_f32_e64 s[56:57], v159, v139
	v_cndmask_b32_e64 v224, 0, 4, s[66:67]
	v_cndmask_b32_e64 v225, 0, 8, vcc
	s_andn2_b64 s[54:55], s[54:55], s[66:67]
	s_andn2_b64 s[56:57], s[56:57], vcc
	v_or3_b32 v228, v228, v224, v225
	v_cmp_ge_f32_e64 s[66:67], v160, v140
	v_cmp_ge_f32_e64 s[58:59], v160, v139
	v_cmp_ge_f32_e32 vcc, v161, v140
	v_cmp_ge_f32_e64 s[60:61], v161, v139
	v_cndmask_b32_e64 v224, 0, v201, s[66:67]
	v_cndmask_b32_e64 v225, 0, v200, vcc
	s_andn2_b64 s[58:59], s[58:59], s[66:67]
	s_andn2_b64 s[60:61], s[60:61], vcc
	v_or3_b32 v228, v228, v224, v225
	v_cmp_ge_f32_e64 s[66:67], v162, v140
	v_cmp_ge_f32_e64 s[62:63], v162, v139
	v_cmp_ge_f32_e32 vcc, v163, v140
	v_cmp_ge_f32_e64 s[64:65], v163, v139
	v_cndmask_b32_e64 v224, 0, v199, s[66:67]
	v_cndmask_b32_e64 v225, 0, v198, vcc
	s_andn2_b64 s[62:63], s[62:63], s[66:67]
	s_andn2_b64 s[64:65], s[64:65], vcc
	v_or3_b32 v228, v228, v224, v225
	v_lshlrev_b32_e32 v104, v143, v228
	ds_bpermute_b32 v105, v144, v104
	v_mov_b32_e32 v227, s96
	s_mov_b64 s[14:15], exec
	s_mov_b64 exec, s[50:51]
	ds_add_rtn_u32 v214, v142, v193
	s_mov_b64 exec, s[52:53]
	ds_add_rtn_u32 v215, v142, v193
	s_mov_b64 exec, s[54:55]
	ds_add_rtn_u32 v216, v142, v193
	s_mov_b64 exec, s[56:57]
	ds_add_rtn_u32 v217, v142, v193
	s_mov_b64 exec, s[58:59]
	ds_add_rtn_u32 v218, v142, v193
	s_mov_b64 exec, s[60:61]
	ds_add_rtn_u32 v219, v142, v193
	s_mov_b64 exec, s[62:63]
	ds_add_rtn_u32 v220, v142, v193
	s_mov_b64 exec, s[64:65]
	ds_add_rtn_u32 v221, v142, v193
	s_mov_b64 exec, s[50:51]
	v_xor_b32_e32 v206, v196, v156
	v_bfe_u32 v222, v206, 11, 10
	v_bfe_u32 v223, v206, 10, 1
	v_lshl_add_u32 v222, v222, 2, v128
	v_mad_u32_u24 v223, v223, v235, 1
	ds_add_u32 v222, v223
	s_mov_b64 exec, s[52:53]
	v_xor_b32_e32 v207, v196, v157
	v_bfe_u32 v222, v207, 11, 10
	v_bfe_u32 v223, v207, 10, 1
	v_lshl_add_u32 v222, v222, 2, v128
	v_mad_u32_u24 v223, v223, v235, 1
	ds_add_u32 v222, v223
	s_mov_b64 exec, s[54:55]
	v_xor_b32_e32 v208, v196, v158
	v_bfe_u32 v222, v208, 11, 10
	v_bfe_u32 v223, v208, 10, 1
	v_lshl_add_u32 v222, v222, 2, v128
	v_mad_u32_u24 v223, v223, v235, 1
	ds_add_u32 v222, v223
	s_mov_b64 exec, s[56:57]
	v_xor_b32_e32 v209, v196, v159
	v_bfe_u32 v222, v209, 11, 10
	v_bfe_u32 v223, v209, 10, 1
	v_lshl_add_u32 v222, v222, 2, v128
	v_mad_u32_u24 v223, v223, v235, 1
	ds_add_u32 v222, v223
	s_waitcnt lgkmcnt(8)
	s_mov_b64 exec, s[58:59]
	v_xor_b32_e32 v210, v196, v160
	v_bfe_u32 v222, v210, 11, 10
	v_bfe_u32 v223, v210, 10, 1
	v_lshl_add_u32 v222, v222, 2, v128
	v_mad_u32_u24 v223, v223, v235, 1
	ds_add_u32 v222, v223
	s_mov_b64 exec, s[60:61]
	v_xor_b32_e32 v211, v196, v161
	v_bfe_u32 v222, v211, 11, 10
	v_bfe_u32 v223, v211, 10, 1
	v_lshl_add_u32 v222, v222, 2, v128
	v_mad_u32_u24 v223, v223, v235, 1
	ds_add_u32 v222, v223
	s_mov_b64 exec, s[62:63]
	v_xor_b32_e32 v212, v196, v162
	v_bfe_u32 v222, v212, 11, 10
	v_bfe_u32 v223, v212, 10, 1
	v_lshl_add_u32 v222, v222, 2, v128
	v_mad_u32_u24 v223, v223, v235, 1
	ds_add_u32 v222, v223
	s_mov_b64 exec, s[64:65]
	v_xor_b32_e32 v213, v196, v163
	v_bfe_u32 v222, v213, 11, 10
	v_bfe_u32 v223, v213, 10, 1
	v_lshl_add_u32 v222, v222, 2, v128
	v_mad_u32_u24 v223, v223, v235, 1
	ds_add_u32 v222, v223
	s_waitcnt lgkmcnt(8)
	s_mov_b64 exec, s[14:15]
	v_or_b32_e32 v104, v105, v104
	ds_bpermute_b32 v105, v145, v104
	s_mov_b64 exec, s[50:51]
	v_cmp_lt_u32_e64 s[66:67], s0, v214
	s_add_i32 s85, s74, 0x0
	v_bfe_u32 v224, v206, 10, 11
	v_lshl_add_u32 v222, v214, 2, v141
	v_add3_u32 v224, v224, v124, s85
	s_andn2_b64 exec, exec, s[66:67]
	ds_write_b32 v222, v224
	s_mov_b64 exec, s[66:67]
	ds_write_b32 v227, v193
	s_mov_b64 exec, s[52:53]
	v_cmp_lt_u32_e64 s[66:67], s0, v215
	s_add_i32 s85, s74, 0x800
	v_bfe_u32 v224, v207, 10, 11
	v_lshl_add_u32 v222, v215, 2, v141
	v_add3_u32 v224, v224, v124, s85
	s_andn2_b64 exec, exec, s[66:67]
	ds_write_b32 v222, v224
	s_mov_b64 exec, s[66:67]
	ds_write_b32 v227, v193
	s_waitcnt lgkmcnt(8)
	s_mov_b64 exec, s[54:55]
	v_cmp_lt_u32_e64 s[66:67], s0, v216
	s_add_i32 s85, s74, 0x1000
	v_bfe_u32 v224, v208, 10, 11
	v_lshl_add_u32 v222, v216, 2, v141
	v_add3_u32 v224, v224, v124, s85
	s_andn2_b64 exec, exec, s[66:67]
	ds_write_b32 v222, v224
	s_mov_b64 exec, s[66:67]
	ds_write_b32 v227, v193
	s_mov_b64 exec, s[56:57]
	v_cmp_lt_u32_e64 s[66:67], s0, v217
	s_add_i32 s85, s74, 0x1800
	v_bfe_u32 v224, v209, 10, 11
	v_lshl_add_u32 v222, v217, 2, v141
	v_add3_u32 v224, v224, v124, s85
	s_andn2_b64 exec, exec, s[66:67]
	ds_write_b32 v222, v224
	s_mov_b64 exec, s[66:67]
	ds_write_b32 v227, v193
	s_waitcnt lgkmcnt(8)
	s_mov_b64 exec, s[58:59]
	v_cmp_lt_u32_e64 s[66:67], s0, v218
	s_add_i32 s85, s74, 0x8000
	v_bfe_u32 v224, v210, 10, 11
	v_lshl_add_u32 v222, v218, 2, v141
	v_add3_u32 v224, v224, v124, s85
	s_andn2_b64 exec, exec, s[66:67]
	ds_write_b32 v222, v224
	s_mov_b64 exec, s[66:67]
	ds_write_b32 v227, v193
	s_mov_b64 exec, s[60:61]
	v_cmp_lt_u32_e64 s[66:67], s0, v219
	s_add_i32 s85, s74, 0x8800
	v_bfe_u32 v224, v211, 10, 11
	v_lshl_add_u32 v222, v219, 2, v141
	v_add3_u32 v224, v224, v124, s85
	s_andn2_b64 exec, exec, s[66:67]
	ds_write_b32 v222, v224
	s_mov_b64 exec, s[66:67]
	ds_write_b32 v227, v193
	s_waitcnt lgkmcnt(8)
	s_mov_b64 exec, s[62:63]
	v_cmp_lt_u32_e64 s[66:67], s0, v220
	s_add_i32 s85, s74, 0x9000
	v_bfe_u32 v224, v212, 10, 11
	v_lshl_add_u32 v222, v220, 2, v141
	v_add3_u32 v224, v224, v124, s85
	s_andn2_b64 exec, exec, s[66:67]
	ds_write_b32 v222, v224
	s_mov_b64 exec, s[66:67]
	ds_write_b32 v227, v193
	s_mov_b64 exec, s[64:65]
	v_cmp_lt_u32_e64 s[66:67], s0, v221
	s_add_i32 s85, s74, 0x9800
	v_bfe_u32 v224, v213, 10, 11
	v_lshl_add_u32 v222, v221, 2, v141
	v_add3_u32 v224, v224, v124, s85
	s_andn2_b64 exec, exec, s[66:67]
	ds_write_b32 v222, v224
	s_mov_b64 exec, s[66:67]
	ds_write_b32 v227, v193
	s_mov_b64 exec, s[14:15]
	s_and_saveexec_b64 s[14:15], s[38:39]
	v_or_b32_e32 v106, v104, v105
	v_lshl_add_u64 v[104:105], v[122:123], 0, s[74:75]
	v_add_co_u32_e32 v104, vcc, 0x3f700000, v104
	s_nop 1
	v_addc_co_u32_e32 v105, vcc, 0, v105, vcc
	global_store_dword v[104:105], v106, off
	s_or_b64 exec, exec, s[14:15]
	s_add_u32 s74, s74, 0x80000
	s_addc_u32 s75, s75, 0
	s_add_i32 s31, s31, 8
	s_cmp_ge_i32 s31, s32
	s_cbranch_scc1 .Lpb2_done

.Lpb2_i3:
	s_add_i32 s85, s31, 32
	s_min_i32 s85, s85, s100
	v_lshl_add_u32 v233, s85, 11, v230
	global_load_dwordx4 v[236:239], v233, s[20:21]
	global_load_dwordx4 v[240:243], v233, s[20:21] offset:1024
	s_waitcnt vmcnt(12)
	v_cmp_ge_f32_e64 s[66:67], v80, v140
	v_cmp_ge_f32_e64 s[50:51], v80, v139
	v_cmp_ge_f32_e32 vcc, v81, v140
	v_cmp_ge_f32_e64 s[52:53], v81, v139
	v_cndmask_b32_e64 v224, 0, 1, s[66:67]
	v_cndmask_b32_e64 v225, 0, 2, vcc
	s_andn2_b64 s[50:51], s[50:51], s[66:67]
	s_andn2_b64 s[52:53], s[52:53], vcc
	v_or_b32_e32 v228, v224, v225
	v_cmp_ge_f32_e64 s[66:67], v82, v140
	v_cmp_ge_f32_e64 s[54:55], v82, v139
	v_cmp_ge_f32_e32 vcc, v83, v140
	v_cmp_ge_f32_e64 s[56:57], v83, v139
	v_cndmask_b32_e64 v224, 0, 4, s[66:67]
	v_cndmask_b32_e64 v225, 0, 8, vcc
	s_andn2_b64 s[54:55], s[54:55], s[66:67]
	s_andn2_b64 s[56:57], s[56:57], vcc
	v_or3_b32 v228, v228, v224, v225
	v_cmp_ge_f32_e64 s[66:67], v84, v140
	v_cmp_ge_f32_e64 s[58:59], v84, v139
	v_cmp_ge_f32_e32 vcc, v85, v140
	v_cmp_ge_f32_e64 s[60:61], v85, v139
	v_cndmask_b32_e64 v224, 0, v201, s[66:67]
	v_cndmask_b32_e64 v225, 0, v200, vcc
	s_andn2_b64 s[58:59], s[58:59], s[66:67]
	s_andn2_b64 s[60:61], s[60:61], vcc
	v_or3_b32 v228, v228, v224, v225
	v_cmp_ge_f32_e64 s[66:67], v86, v140
	v_cmp_ge_f32_e64 s[62:63], v86, v139
	v_cmp_ge_f32_e32 vcc, v87, v140
	v_cmp_ge_f32_e64 s[64:65], v87, v139
	v_cndmask_b32_e64 v224, 0, v199, s[66:67]
	v_cndmask_b32_e64 v225, 0, v198, vcc
	s_andn2_b64 s[62:63], s[62:63], s[66:67]
	s_andn2_b64 s[64:65], s[64:65], vcc
	v_or3_b32 v228, v228, v224, v225
	v_lshlrev_b32_e32 v104, v143, v228
	ds_bpermute_b32 v105, v144, v104
	v_mov_b32_e32 v227, s96
	s_mov_b64 s[14:15], exec
	s_mov_b64 exec, s[50:51]
	ds_add_rtn_u32 v214, v142, v193
	s_mov_b64 exec, s[52:53]
	ds_add_rtn_u32 v215, v142, v193
	s_mov_b64 exec, s[54:55]
	ds_add_rtn_u32 v216, v142, v193
	s_mov_b64 exec, s[56:57]
	ds_add_rtn_u32 v217, v142, v193
	s_mov_b64 exec, s[58:59]
	ds_add_rtn_u32 v218, v142, v193
	s_mov_b64 exec, s[60:61]
	ds_add_rtn_u32 v219, v142, v193
	s_mov_b64 exec, s[62:63]
	ds_add_rtn_u32 v220, v142, v193
	s_mov_b64 exec, s[64:65]
	ds_add_rtn_u32 v221, v142, v193
	s_mov_b64 exec, s[50:51]
	v_xor_b32_e32 v206, v196, v80
	v_bfe_u32 v222, v206, 11, 10
	v_bfe_u32 v223, v206, 10, 1
	v_lshl_add_u32 v222, v222, 2, v128
	v_mad_u32_u24 v223, v223, v235, 1
	ds_add_u32 v222, v223
	s_mov_b64 exec, s[52:53]
	v_xor_b32_e32 v207, v196, v81
	v_bfe_u32 v222, v207, 11, 10
	v_bfe_u32 v223, v207, 10, 1
	v_lshl_add_u32 v222, v222, 2, v128
	v_mad_u32_u24 v223, v223, v235, 1
	ds_add_u32 v222, v223
	s_mov_b64 exec, s[54:55]
	v_xor_b32_e32 v208, v196, v82
	v_bfe_u32 v222, v208, 11, 10
	v_bfe_u32 v223, v208, 10, 1
	v_lshl_add_u32 v222, v222, 2, v128
	v_mad_u32_u24 v223, v223, v235, 1
	ds_add_u32 v222, v223
	s_mov_b64 exec, s[56:57]
	v_xor_b32_e32 v209, v196, v83
	v_bfe_u32 v222, v209, 11, 10
	v_bfe_u32 v223, v209, 10, 1
	v_lshl_add_u32 v222, v222, 2, v128
	v_mad_u32_u24 v223, v223, v235, 1
	ds_add_u32 v222, v223
	s_waitcnt lgkmcnt(8)
	s_mov_b64 exec, s[58:59]
	v_xor_b32_e32 v210, v196, v84
	v_bfe_u32 v222, v210, 11, 10
	v_bfe_u32 v223, v210, 10, 1
	v_lshl_add_u32 v222, v222, 2, v128
	v_mad_u32_u24 v223, v223, v235, 1
	ds_add_u32 v222, v223
	s_mov_b64 exec, s[60:61]
	v_xor_b32_e32 v211, v196, v85
	v_bfe_u32 v222, v211, 11, 10
	v_bfe_u32 v223, v211, 10, 1
	v_lshl_add_u32 v222, v222, 2, v128
	v_mad_u32_u24 v223, v223, v235, 1
	ds_add_u32 v222, v223
	s_mov_b64 exec, s[62:63]
	v_xor_b32_e32 v212, v196, v86
	v_bfe_u32 v222, v212, 11, 10
	v_bfe_u32 v223, v212, 10, 1
	v_lshl_add_u32 v222, v222, 2, v128
	v_mad_u32_u24 v223, v223, v235, 1
	ds_add_u32 v222, v223
	s_mov_b64 exec, s[64:65]
	v_xor_b32_e32 v213, v196, v87
	v_bfe_u32 v222, v213, 11, 10
	v_bfe_u32 v223, v213, 10, 1
	v_lshl_add_u32 v222, v222, 2, v128
	v_mad_u32_u24 v223, v223, v235, 1
	ds_add_u32 v222, v223
	s_waitcnt lgkmcnt(8)
	s_mov_b64 exec, s[14:15]
	v_or_b32_e32 v104, v105, v104
	ds_bpermute_b32 v105, v145, v104
	s_mov_b64 exec, s[50:51]
	v_cmp_lt_u32_e64 s[66:67], s0, v214
	s_add_i32 s85, s74, 0x0
	v_bfe_u32 v224, v206, 10, 11
	v_lshl_add_u32 v222, v214, 2, v141
	v_add3_u32 v224, v224, v124, s85
	s_andn2_b64 exec, exec, s[66:67]
	ds_write_b32 v222, v224
	s_mov_b64 exec, s[66:67]
	ds_write_b32 v227, v193
	s_mov_b64 exec, s[52:53]
	v_cmp_lt_u32_e64 s[66:67], s0, v215
	s_add_i32 s85, s74, 0x800
	v_bfe_u32 v224, v207, 10, 11
	v_lshl_add_u32 v222, v215, 2, v141
	v_add3_u32 v224, v224, v124, s85
	s_andn2_b64 exec, exec, s[66:67]
	ds_write_b32 v222, v224
	s_mov_b64 exec, s[66:67]
	ds_write_b32 v227, v193
	s_waitcnt lgkmcnt(8)
	s_mov_b64 exec, s[54:55]
	v_cmp_lt_u32_e64 s[66:67], s0, v216
	s_add_i32 s85, s74, 0x1000
	v_bfe_u32 v224, v208, 10, 11
	v_lshl_add_u32 v222, v216, 2, v141
	v_add3_u32 v224, v224, v124, s85
	s_andn2_b64 exec, exec, s[66:67]
	ds_write_b32 v222, v224
	s_mov_b64 exec, s[66:67]
	ds_write_b32 v227, v193
	s_mov_b64 exec, s[56:57]
	v_cmp_lt_u32_e64 s[66:67], s0, v217
	s_add_i32 s85, s74, 0x1800
	v_bfe_u32 v224, v209, 10, 11
	v_lshl_add_u32 v222, v217, 2, v141
	v_add3_u32 v224, v224, v124, s85
	s_andn2_b64 exec, exec, s[66:67]
	ds_write_b32 v222, v224
	s_mov_b64 exec, s[66:67]
	ds_write_b32 v227, v193
	s_waitcnt lgkmcnt(8)
	s_mov_b64 exec, s[58:59]
	v_cmp_lt_u32_e64 s[66:67], s0, v218
	s_add_i32 s85, s74, 0x8000
	v_bfe_u32 v224, v210, 10, 11
	v_lshl_add_u32 v222, v218, 2, v141
	v_add3_u32 v224, v224, v124, s85
	s_andn2_b64 exec, exec, s[66:67]
	ds_write_b32 v222, v224
	s_mov_b64 exec, s[66:67]
	ds_write_b32 v227, v193
	s_mov_b64 exec, s[60:61]
	v_cmp_lt_u32_e64 s[66:67], s0, v219
	s_add_i32 s85, s74, 0x8800
	v_bfe_u32 v224, v211, 10, 11
	v_lshl_add_u32 v222, v219, 2, v141
	v_add3_u32 v224, v224, v124, s85
	s_andn2_b64 exec, exec, s[66:67]
	ds_write_b32 v222, v224
	s_mov_b64 exec, s[66:67]
	ds_write_b32 v227, v193
	s_waitcnt lgkmcnt(8)
	s_mov_b64 exec, s[62:63]
	v_cmp_lt_u32_e64 s[66:67], s0, v220
	s_add_i32 s85, s74, 0x9000
	v_bfe_u32 v224, v212, 10, 11
	v_lshl_add_u32 v222, v220, 2, v141
	v_add3_u32 v224, v224, v124, s85
	s_andn2_b64 exec, exec, s[66:67]
	ds_write_b32 v222, v224
	s_mov_b64 exec, s[66:67]
	ds_write_b32 v227, v193
	s_mov_b64 exec, s[64:65]
	v_cmp_lt_u32_e64 s[66:67], s0, v221
	s_add_i32 s85, s74, 0x9800
	v_bfe_u32 v224, v213, 10, 11
	v_lshl_add_u32 v222, v221, 2, v141
	v_add3_u32 v224, v224, v124, s85
	s_andn2_b64 exec, exec, s[66:67]
	ds_write_b32 v222, v224
	s_mov_b64 exec, s[66:67]
	ds_write_b32 v227, v193
	s_mov_b64 exec, s[14:15]
	s_and_saveexec_b64 s[14:15], s[38:39]
	v_or_b32_e32 v106, v104, v105
	v_lshl_add_u64 v[104:105], v[122:123], 0, s[74:75]
	v_add_co_u32_e32 v104, vcc, 0x3f700000, v104
	s_nop 1
	v_addc_co_u32_e32 v105, vcc, 0, v105, vcc
	global_store_dword v[104:105], v106, off
	s_or_b64 exec, exec, s[14:15]
	s_add_u32 s74, s74, 0x80000
	s_addc_u32 s75, s75, 0
	s_add_i32 s31, s31, 8
	s_cmp_ge_i32 s31, s32
	s_cbranch_scc1 .Lpb2_done
.Lpb2_i4:
	s_add_i32 s85, s31, 32
	s_min_i32 s85, s85, s100
	v_lshl_add_u32 v233, s85, 11, v230
	global_load_dwordx4 v[80:83], v233, s[20:21]
	global_load_dwordx4 v[84:87], v233, s[20:21] offset:1024
	s_waitcnt vmcnt(12)
	v_cmp_ge_f32_e64 s[66:67], v72, v140
	v_cmp_ge_f32_e64 s[50:51], v72, v139
	v_cmp_ge_f32_e32 vcc, v73, v140
	v_cmp_ge_f32_e64 s[52:53], v73, v139
	v_cndmask_b32_e64 v224, 0, 1, s[66:67]
	v_cndmask_b32_e64 v225, 0, 2, vcc
	s_andn2_b64 s[50:51], s[50:51], s[66:67]
	s_andn2_b64 s[52:53], s[52:53], vcc
	v_or_b32_e32 v228, v224, v225
	v_cmp_ge_f32_e64 s[66:67], v74, v140
	v_cmp_ge_f32_e64 s[54:55], v74, v139
	v_cmp_ge_f32_e32 vcc, v75, v140
	v_cmp_ge_f32_e64 s[56:57], v75, v139
	v_cndmask_b32_e64 v224, 0, 4, s[66:67]
	v_cndmask_b32_e64 v225, 0, 8, vcc
	s_andn2_b64 s[54:55], s[54:55], s[66:67]
	s_andn2_b64 s[56:57], s[56:57], vcc
	v_or3_b32 v228, v228, v224, v225
	v_cmp_ge_f32_e64 s[66:67], v76, v140
	v_cmp_ge_f32_e64 s[58:59], v76, v139
	v_cmp_ge_f32_e32 vcc, v77, v140
	v_cmp_ge_f32_e64 s[60:61], v77, v139
	v_cndmask_b32_e64 v224, 0, v201, s[66:67]
	v_cndmask_b32_e64 v225, 0, v200, vcc
	s_andn2_b64 s[58:59], s[58:59], s[66:67]
	s_andn2_b64 s[60:61], s[60:61], vcc
	v_or3_b32 v228, v228, v224, v225
	v_cmp_ge_f32_e64 s[66:67], v78, v140
	v_cmp_ge_f32_e64 s[62:63], v78, v139
	v_cmp_ge_f32_e32 vcc, v79, v140
	v_cmp_ge_f32_e64 s[64:65], v79, v139
	v_cndmask_b32_e64 v224, 0, v199, s[66:67]
	v_cndmask_b32_e64 v225, 0, v198, vcc
	s_andn2_b64 s[62:63], s[62:63], s[66:67]
	s_andn2_b64 s[64:65], s[64:65], vcc
	v_or3_b32 v228, v228, v224, v225
	v_lshlrev_b32_e32 v104, v143, v228
	ds_bpermute_b32 v105, v144, v104
	v_mov_b32_e32 v227, s96
	s_mov_b64 s[14:15], exec
	s_mov_b64 exec, s[50:51]
	ds_add_rtn_u32 v214, v142, v193
	s_mov_b64 exec, s[52:53]
	ds_add_rtn_u32 v215, v142, v193
	s_mov_b64 exec, s[54:55]
	ds_add_rtn_u32 v216, v142, v193
	s_mov_b64 exec, s[56:57]
	ds_add_rtn_u32 v217, v142, v193
	s_mov_b64 exec, s[58:59]
	ds_add_rtn_u32 v218, v142, v193
	s_mov_b64 exec, s[60:61]
	ds_add_rtn_u32 v219, v142, v193
	s_mov_b64 exec, s[62:63]
	ds_add_rtn_u32 v220, v142, v193
	s_mov_b64 exec, s[64:65]
	ds_add_rtn_u32 v221, v142, v193
	s_mov_b64 exec, s[50:51]
	v_xor_b32_e32 v206, v196, v72
	v_bfe_u32 v222, v206, 11, 10
	v_bfe_u32 v223, v206, 10, 1
	v_lshl_add_u32 v222, v222, 2, v128
	v_mad_u32_u24 v223, v223, v235, 1
	ds_add_u32 v222, v223
	s_mov_b64 exec, s[52:53]
	v_xor_b32_e32 v207, v196, v73
	v_bfe_u32 v222, v207, 11, 10
	v_bfe_u32 v223, v207, 10, 1
	v_lshl_add_u32 v222, v222, 2, v128
	v_mad_u32_u24 v223, v223, v235, 1
	ds_add_u32 v222, v223
	s_mov_b64 exec, s[54:55]
	v_xor_b32_e32 v208, v196, v74
	v_bfe_u32 v222, v208, 11, 10
	v_bfe_u32 v223, v208, 10, 1
	v_lshl_add_u32 v222, v222, 2, v128
	v_mad_u32_u24 v223, v223, v235, 1
	ds_add_u32 v222, v223
	s_mov_b64 exec, s[56:57]
	v_xor_b32_e32 v209, v196, v75
	v_bfe_u32 v222, v209, 11, 10
	v_bfe_u32 v223, v209, 10, 1
	v_lshl_add_u32 v222, v222, 2, v128
	v_mad_u32_u24 v223, v223, v235, 1
	ds_add_u32 v222, v223
	s_waitcnt lgkmcnt(8)
	s_mov_b64 exec, s[58:59]
	v_xor_b32_e32 v210, v196, v76
	v_bfe_u32 v222, v210, 11, 10
	v_bfe_u32 v223, v210, 10, 1
	v_lshl_add_u32 v222, v222, 2, v128
	v_mad_u32_u24 v223, v223, v235, 1
	ds_add_u32 v222, v223
	s_mov_b64 exec, s[60:61]
	v_xor_b32_e32 v211, v196, v77
	v_bfe_u32 v222, v211, 11, 10
	v_bfe_u32 v223, v211, 10, 1
	v_lshl_add_u32 v222, v222, 2, v128
	v_mad_u32_u24 v223, v223, v235, 1
	ds_add_u32 v222, v223
	s_mov_b64 exec, s[62:63]
	v_xor_b32_e32 v212, v196, v78
	v_bfe_u32 v222, v212, 11, 10
	v_bfe_u32 v223, v212, 10, 1
	v_lshl_add_u32 v222, v222, 2, v128
	v_mad_u32_u24 v223, v223, v235, 1
	ds_add_u32 v222, v223
	s_mov_b64 exec, s[64:65]
	v_xor_b32_e32 v213, v196, v79
	v_bfe_u32 v222, v213, 11, 10
	v_bfe_u32 v223, v213, 10, 1
	v_lshl_add_u32 v222, v222, 2, v128
	v_mad_u32_u24 v223, v223, v235, 1
	ds_add_u32 v222, v223
	s_waitcnt lgkmcnt(8)
	s_mov_b64 exec, s[14:15]
	v_or_b32_e32 v104, v105, v104
	ds_bpermute_b32 v105, v145, v104
	s_mov_b64 exec, s[50:51]
	v_cmp_lt_u32_e64 s[66:67], s0, v214
	s_add_i32 s85, s74, 0x0
	v_bfe_u32 v224, v206, 10, 11
	v_lshl_add_u32 v222, v214, 2, v141
	v_add3_u32 v224, v224, v124, s85
	s_andn2_b64 exec, exec, s[66:67]
	ds_write_b32 v222, v224
	s_mov_b64 exec, s[66:67]
	ds_write_b32 v227, v193
	s_mov_b64 exec, s[52:53]
	v_cmp_lt_u32_e64 s[66:67], s0, v215
	s_add_i32 s85, s74, 0x800
	v_bfe_u32 v224, v207, 10, 11
	v_lshl_add_u32 v222, v215, 2, v141
	v_add3_u32 v224, v224, v124, s85
	s_andn2_b64 exec, exec, s[66:67]
	ds_write_b32 v222, v224
	s_mov_b64 exec, s[66:67]
	ds_write_b32 v227, v193
	s_waitcnt lgkmcnt(8)
	s_mov_b64 exec, s[54:55]
	v_cmp_lt_u32_e64 s[66:67], s0, v216
	s_add_i32 s85, s74, 0x1000
	v_bfe_u32 v224, v208, 10, 11
	v_lshl_add_u32 v222, v216, 2, v141
	v_add3_u32 v224, v224, v124, s85
	s_andn2_b64 exec, exec, s[66:67]
	ds_write_b32 v222, v224
	s_mov_b64 exec, s[66:67]
	ds_write_b32 v227, v193
	s_mov_b64 exec, s[56:57]
	v_cmp_lt_u32_e64 s[66:67], s0, v217
	s_add_i32 s85, s74, 0x1800
	v_bfe_u32 v224, v209, 10, 11
	v_lshl_add_u32 v222, v217, 2, v141
	v_add3_u32 v224, v224, v124, s85
	s_andn2_b64 exec, exec, s[66:67]
	ds_write_b32 v222, v224
	s_mov_b64 exec, s[66:67]
	ds_write_b32 v227, v193
	s_waitcnt lgkmcnt(8)
	s_mov_b64 exec, s[58:59]
	v_cmp_lt_u32_e64 s[66:67], s0, v218
	s_add_i32 s85, s74, 0x8000
	v_bfe_u32 v224, v210, 10, 11
	v_lshl_add_u32 v222, v218, 2, v141
	v_add3_u32 v224, v224, v124, s85
	s_andn2_b64 exec, exec, s[66:67]
	ds_write_b32 v222, v224
	s_mov_b64 exec, s[66:67]
	ds_write_b32 v227, v193
	s_mov_b64 exec, s[60:61]
	v_cmp_lt_u32_e64 s[66:67], s0, v219
	s_add_i32 s85, s74, 0x8800
	v_bfe_u32 v224, v211, 10, 11
	v_lshl_add_u32 v222, v219, 2, v141
	v_add3_u32 v224, v224, v124, s85
	s_andn2_b64 exec, exec, s[66:67]
	ds_write_b32 v222, v224
	s_mov_b64 exec, s[66:67]
	ds_write_b32 v227, v193
	s_waitcnt lgkmcnt(8)
	s_mov_b64 exec, s[62:63]
	v_cmp_lt_u32_e64 s[66:67], s0, v220
	s_add_i32 s85, s74, 0x9000
	v_bfe_u32 v224, v212, 10, 11
	v_lshl_add_u32 v222, v220, 2, v141
	v_add3_u32 v224, v224, v124, s85
	s_andn2_b64 exec, exec, s[66:67]
	ds_write_b32 v222, v224
	s_mov_b64 exec, s[66:67]
	ds_write_b32 v227, v193
	s_mov_b64 exec, s[64:65]
	v_cmp_lt_u32_e64 s[66:67], s0, v221
	s_add_i32 s85, s74, 0x9800
	v_bfe_u32 v224, v213, 10, 11
	v_lshl_add_u32 v222, v221, 2, v141
	v_add3_u32 v224, v224, v124, s85
	s_andn2_b64 exec, exec, s[66:67]
	ds_write_b32 v222, v224
	s_mov_b64 exec, s[66:67]
	ds_write_b32 v227, v193
	s_mov_b64 exec, s[14:15]
	s_and_saveexec_b64 s[14:15], s[38:39]
	v_or_b32_e32 v106, v104, v105
	v_lshl_add_u64 v[104:105], v[122:123], 0, s[74:75]
	v_add_co_u32_e32 v104, vcc, 0x3f700000, v104
	s_nop 1
	v_addc_co_u32_e32 v105, vcc, 0, v105, vcc
	global_store_dword v[104:105], v106, off
	s_or_b64 exec, exec, s[14:15]
	s_add_u32 s74, s74, 0x80000
	s_addc_u32 s75, s75, 0
	s_add_i32 s31, s31, 8
	s_cmp_ge_i32 s31, s32
	s_cbranch_scc0 .Lpb2_i0

.LBB0_1438:
	s_waitcnt vmcnt(3) lgkmcnt(0)
	v_mfma_f32_16x16x32_bf16 v[146:149], v[116:119], v[0:3], 0
	v_mfma_f32_16x16x32_bf16 v[178:181], v[116:119], v[244:247], 0
	s_add_i32 s85, s31, 8
	s_min_i32 s14, s85, s72
	v_lshl_or_b32 v72, s14, 5, v125
	s_waitcnt vmcnt(1)
	v_mfma_f32_16x16x32_bf16 v[150:153], v[112:115], v[0:3], 0
	v_mfma_f32_16x16x32_bf16 v[182:185], v[112:115], v[244:247], 0
	v_ashrrev_i32_e32 v73, 31, v72
	v_lshlrev_b64 v[72:73], 7, v[72:73]
	v_sub_u32_e32 v72, v72, v229
	v_lshl_add_u64 v[84:85], v[120:121], 0, v[72:73]
	v_mfma_f32_16x16x32_bf16 v[154:157], v[108:111], v[4:7], v[146:149]
	v_mfma_f32_16x16x32_bf16 v[178:181], v[108:111], v[248:251], v[178:181]
	global_load_dwordx4 v[72:75], v[84:85], off
	global_load_dwordx4 v[76:79], v[84:85], off offset:1024
	global_load_dwordx4 v[80:83], v[84:85], off offset:2048
	s_nop 0
	global_load_dwordx4 v[84:87], v[84:85], off offset:3072
	s_nop 0
	s_nop 0
	s_waitcnt vmcnt(4)
	v_mfma_f32_16x16x32_bf16 v[158:161], v[104:107], v[4:7], v[150:153]
	v_mfma_f32_16x16x32_bf16 v[182:185], v[104:107], v[248:251], v[182:185]
	v_mfma_f32_16x16x32_bf16 v[146:149], v[116:119], v[16:19], 0
	v_mfma_f32_16x16x32_bf16 v[150:153], v[112:115], v[16:19], 0
	v_mfma_f32_16x16x32_bf16 v[146:149], v[108:111], v[20:23], v[146:149]
	v_mfma_f32_16x16x32_bf16 v[150:153], v[104:107], v[20:23], v[150:153]
	s_nop 3
	v_fma_f32 v178, v12, |v154|, v178
	v_fma_f32 v182, v12, |v158|, v182
	v_fma_f32 v179, v12, |v155|, v179
	v_fma_f32 v183, v12, |v159|, v183
	v_fma_f32 v180, v12, |v156|, v180
	v_fma_f32 v184, v12, |v160|, v184
	v_fma_f32 v181, v12, |v157|, v181
	v_fma_f32 v185, v12, |v161|, v185
	v_mfma_f32_16x16x32_bf16 v[154:157], v[116:119], v[24:27], 0
	v_mfma_f32_16x16x32_bf16 v[158:161], v[112:115], v[24:27], 0
	v_mfma_f32_16x16x32_bf16 v[154:157], v[108:111], v[28:31], v[154:157]
	v_mfma_f32_16x16x32_bf16 v[158:161], v[104:107], v[28:31], v[158:161]
	s_nop 3
	v_fma_f32 v178, v13, |v146|, v178
	v_fma_f32 v182, v13, |v150|, v182
	v_fma_f32 v179, v13, |v147|, v179
	v_fma_f32 v183, v13, |v151|, v183
	v_fma_f32 v180, v13, |v148|, v180
	v_fma_f32 v184, v13, |v152|, v184
	v_fma_f32 v181, v13, |v149|, v181
	v_fma_f32 v185, v13, |v153|, v185
	v_mfma_f32_16x16x32_bf16 v[146:149], v[116:119], v[32:35], 0
	v_mfma_f32_16x16x32_bf16 v[150:153], v[112:115], v[32:35], 0
	v_mfma_f32_16x16x32_bf16 v[146:149], v[108:111], v[36:39], v[146:149]
	v_mfma_f32_16x16x32_bf16 v[150:153], v[104:107], v[36:39], v[150:153]
	s_nop 3
	v_fma_f32 v178, v14, |v154|, v178
	v_fma_f32 v182, v14, |v158|, v182
	v_fma_f32 v179, v14, |v155|, v179
	v_fma_f32 v183, v14, |v159|, v183
	v_fma_f32 v180, v14, |v156|, v180
	v_fma_f32 v184, v14, |v160|, v184
	v_fma_f32 v181, v14, |v157|, v181
	v_fma_f32 v185, v14, |v161|, v185
	v_mfma_f32_16x16x32_bf16 v[154:157], v[116:119], v[40:43], 0
	v_mfma_f32_16x16x32_bf16 v[158:161], v[112:115], v[40:43], 0
	v_mfma_f32_16x16x32_bf16 v[154:157], v[108:111], v[44:47], v[154:157]
	v_mfma_f32_16x16x32_bf16 v[158:161], v[104:107], v[44:47], v[158:161]
	s_nop 3
	v_fma_f32 v178, v15, |v146|, v178
	v_fma_f32 v182, v15, |v150|, v182
	v_fma_f32 v179, v15, |v147|, v179
	v_fma_f32 v183, v15, |v151|, v183
	v_fma_f32 v180, v15, |v148|, v180
	v_fma_f32 v184, v15, |v152|, v184
	v_fma_f32 v181, v15, |v149|, v181
	v_fma_f32 v185, v15, |v153|, v185
	v_mfma_f32_16x16x32_bf16 v[146:149], v[116:119], v[48:51], 0
	v_mfma_f32_16x16x32_bf16 v[150:153], v[112:115], v[48:51], 0
	v_mfma_f32_16x16x32_bf16 v[146:149], v[108:111], v[52:55], v[146:149]
	v_mfma_f32_16x16x32_bf16 v[150:153], v[104:107], v[52:55], v[150:153]
	s_nop 3
	v_fma_f32 v178, v8, |v154|, v178
	v_fma_f32 v182, v8, |v158|, v182
	v_fma_f32 v179, v8, |v155|, v179
	v_fma_f32 v183, v8, |v159|, v183
	v_fma_f32 v180, v8, |v156|, v180
	v_fma_f32 v184, v8, |v160|, v184
	v_fma_f32 v181, v8, |v157|, v181
	v_fma_f32 v185, v8, |v161|, v185
	v_mfma_f32_16x16x32_bf16 v[154:157], v[116:119], v[56:59], 0
	v_mfma_f32_16x16x32_bf16 v[158:161], v[112:115], v[56:59], 0
	v_mfma_f32_16x16x32_bf16 v[154:157], v[108:111], v[60:63], v[154:157]
	v_mfma_f32_16x16x32_bf16 v[158:161], v[104:107], v[60:63], v[158:161]
	s_nop 3
	v_fma_f32 v178, v9, |v146|, v178
	v_fma_f32 v182, v9, |v150|, v182
	v_fma_f32 v179, v9, |v147|, v179
	v_fma_f32 v183, v9, |v151|, v183
	v_fma_f32 v180, v9, |v148|, v180
	v_fma_f32 v184, v9, |v152|, v184
	v_fma_f32 v181, v9, |v149|, v181
	v_fma_f32 v185, v9, |v153|, v185
	v_mfma_f32_16x16x32_bf16 v[146:149], v[116:119], v[64:67], 0
	v_mfma_f32_16x16x32_bf16 v[150:153], v[112:115], v[64:67], 0
	v_mfma_f32_16x16x32_bf16 v[146:149], v[108:111], v[68:71], v[146:149]
	v_mfma_f32_16x16x32_bf16 v[150:153], v[104:107], v[68:71], v[150:153]
	s_nop 3
	v_fma_f32 v178, v10, |v154|, v178
	v_fma_f32 v182, v10, |v158|, v182
	v_fma_f32 v179, v10, |v155|, v179
	v_fma_f32 v183, v10, |v159|, v183
	v_fma_f32 v180, v10, |v156|, v180
	v_fma_f32 v184, v10, |v160|, v184
	v_fma_f32 v181, v10, |v157|, v181
	v_fma_f32 v185, v10, |v161|, v185
	s_nop 7
	v_fma_f32 v178, v11, |v146|, v178
	v_fma_f32 v182, v11, |v150|, v182
	v_fma_f32 v179, v11, |v147|, v179
	v_fma_f32 v183, v11, |v151|, v183
	v_fma_f32 v180, v11, |v148|, v180
	v_fma_f32 v184, v11, |v152|, v184
	v_fma_f32 v181, v11, |v149|, v181
	v_fma_f32 v185, v11, |v153|, v185
	v_cmp_ge_f32_e64 s[66:67], v178, v140
	v_cmp_ge_f32_e64 s[50:51], v178, v139
	v_cmp_ge_f32_e32 vcc, v179, v140
	v_cmp_ge_f32_e64 s[52:53], v179, v139
	v_cndmask_b32_e64 v224, 0, 1, s[66:67]
	v_cndmask_b32_e64 v225, 0, 2, vcc
	s_andn2_b64 s[50:51], s[50:51], s[66:67]
	s_andn2_b64 s[52:53], s[52:53], vcc
	v_or_b32_e32 v228, v224, v225
	v_cmp_ge_f32_e64 s[66:67], v180, v140
	v_cmp_ge_f32_e64 s[54:55], v180, v139
	v_cmp_ge_f32_e32 vcc, v181, v140
	v_cmp_ge_f32_e64 s[56:57], v181, v139
	v_cndmask_b32_e64 v224, 0, 4, s[66:67]
	v_cndmask_b32_e64 v225, 0, 8, vcc
	s_andn2_b64 s[54:55], s[54:55], s[66:67]
	s_andn2_b64 s[56:57], s[56:57], vcc
	v_or3_b32 v228, v228, v224, v225
	v_cmp_ge_f32_e64 s[66:67], v182, v140
	v_cmp_ge_f32_e64 s[58:59], v182, v139
	v_cmp_ge_f32_e32 vcc, v183, v140
	v_cmp_ge_f32_e64 s[60:61], v183, v139
	v_cndmask_b32_e64 v224, 0, v201, s[66:67]
	v_cndmask_b32_e64 v225, 0, v200, vcc
	s_andn2_b64 s[58:59], s[58:59], s[66:67]
	s_andn2_b64 s[60:61], s[60:61], vcc
	v_or3_b32 v228, v228, v224, v225
	v_cmp_ge_f32_e64 s[66:67], v184, v140
	v_cmp_ge_f32_e64 s[62:63], v184, v139
	v_cmp_ge_f32_e32 vcc, v185, v140
	v_cmp_ge_f32_e64 s[64:65], v185, v139
	v_cndmask_b32_e64 v224, 0, v199, s[66:67]
	v_cndmask_b32_e64 v225, 0, v198, vcc
	s_andn2_b64 s[62:63], s[62:63], s[66:67]
	s_andn2_b64 s[64:65], s[64:65], vcc
	v_or3_b32 v228, v228, v224, v225
	v_add_u32_e32 v226, s74, v124
	v_mov_b32_e32 v227, s96
	s_mov_b64 s[14:15], exec
	s_mov_b64 exec, s[50:51]
	v_ashrrev_i32_e32 v206, 31, v178
	v_xor_b32_e32 v206, v206, v178
	v_lshrrev_b32_e32 v222, 9, v206
	v_lshrrev_b32_e32 v223, 6, v206
	v_and_b32_e32 v222, 0xffc, v222
	v_and_b32_e32 v223, 16, v223
	v_add_u32_e32 v222, v128, v222
	v_lshlrev_b32_e64 v223, v223, 1
	ds_add_u32 v222, v223
	s_mov_b64 exec, s[52:53]
	v_ashrrev_i32_e32 v207, 31, v179
	v_xor_b32_e32 v207, v207, v179
	v_lshrrev_b32_e32 v222, 9, v207
	v_lshrrev_b32_e32 v223, 6, v207
	v_and_b32_e32 v222, 0xffc, v222
	v_and_b32_e32 v223, 16, v223
	v_add_u32_e32 v222, v128, v222
	v_lshlrev_b32_e64 v223, v223, 1
	ds_add_u32 v222, v223
	s_mov_b64 exec, s[54:55]
	v_ashrrev_i32_e32 v208, 31, v180
	v_xor_b32_e32 v208, v208, v180
	v_lshrrev_b32_e32 v222, 9, v208
	v_lshrrev_b32_e32 v223, 6, v208
	v_and_b32_e32 v222, 0xffc, v222
	v_and_b32_e32 v223, 16, v223
	v_add_u32_e32 v222, v128, v222
	v_lshlrev_b32_e64 v223, v223, 1
	ds_add_u32 v222, v223
	s_mov_b64 exec, s[56:57]
	v_ashrrev_i32_e32 v209, 31, v181
	v_xor_b32_e32 v209, v209, v181
	v_lshrrev_b32_e32 v222, 9, v209
	v_lshrrev_b32_e32 v223, 6, v209
	v_and_b32_e32 v222, 0xffc, v222
	v_and_b32_e32 v223, 16, v223
	v_add_u32_e32 v222, v128, v222
	v_lshlrev_b32_e64 v223, v223, 1
	ds_add_u32 v222, v223
	s_mov_b64 exec, s[58:59]
	v_ashrrev_i32_e32 v210, 31, v182
	v_xor_b32_e32 v210, v210, v182
	v_lshrrev_b32_e32 v222, 9, v210
	v_lshrrev_b32_e32 v223, 6, v210
	v_and_b32_e32 v222, 0xffc, v222
	v_and_b32_e32 v223, 16, v223
	v_add_u32_e32 v222, v128, v222
	v_lshlrev_b32_e64 v223, v223, 1
	ds_add_u32 v222, v223
	s_mov_b64 exec, s[60:61]
	v_ashrrev_i32_e32 v211, 31, v183
	v_xor_b32_e32 v211, v211, v183
	v_lshrrev_b32_e32 v222, 9, v211
	v_lshrrev_b32_e32 v223, 6, v211
	v_and_b32_e32 v222, 0xffc, v222
	v_and_b32_e32 v223, 16, v223
	v_add_u32_e32 v222, v128, v222
	v_lshlrev_b32_e64 v223, v223, 1
	ds_add_u32 v222, v223
	s_mov_b64 exec, s[62:63]
	v_ashrrev_i32_e32 v212, 31, v184
	v_xor_b32_e32 v212, v212, v184
	v_lshrrev_b32_e32 v222, 9, v212
	v_lshrrev_b32_e32 v223, 6, v212
	v_and_b32_e32 v222, 0xffc, v222
	v_and_b32_e32 v223, 16, v223
	v_add_u32_e32 v222, v128, v222
	v_lshlrev_b32_e64 v223, v223, 1
	ds_add_u32 v222, v223
	s_mov_b64 exec, s[64:65]
	v_ashrrev_i32_e32 v213, 31, v185
	v_xor_b32_e32 v213, v213, v185
	v_lshrrev_b32_e32 v222, 9, v213
	v_lshrrev_b32_e32 v223, 6, v213
	v_and_b32_e32 v222, 0xffc, v222
	v_and_b32_e32 v223, 16, v223
	v_add_u32_e32 v222, v128, v222
	v_lshlrev_b32_e64 v223, v223, 1
	ds_add_u32 v222, v223
	s_waitcnt lgkmcnt(6)
	s_mov_b64 exec, s[50:51]
	ds_add_rtn_u32 v214, v142, v193
	s_mov_b64 exec, s[52:53]
	ds_add_rtn_u32 v215, v142, v193
	s_mov_b64 exec, s[54:55]
	ds_add_rtn_u32 v216, v142, v193
	s_mov_b64 exec, s[56:57]
	ds_add_rtn_u32 v217, v142, v193
	s_mov_b64 exec, s[58:59]
	ds_add_rtn_u32 v218, v142, v193
	s_mov_b64 exec, s[60:61]
	ds_add_rtn_u32 v219, v142, v193
	s_mov_b64 exec, s[62:63]
	ds_add_rtn_u32 v220, v142, v193
	s_mov_b64 exec, s[64:65]
	ds_add_rtn_u32 v221, v142, v193
	s_waitcnt lgkmcnt(0)
	s_mov_b64 exec, s[50:51]
	v_cmp_lt_u32_e64 s[66:67], s0, v214
	v_bfe_u32 v224, v206, 10, 11
	v_add_u32_e32 v225, 0x0, v226
	v_lshl_add_u32 v222, v214, 2, v141
	v_add_u32_e32 v224, v225, v224
	s_andn2_b64 exec, exec, s[66:67]
	ds_write_b32 v222, v224
	s_mov_b64 exec, s[66:67]
	ds_write_b32 v227, v193
	s_mov_b64 exec, s[52:53]
	v_cmp_lt_u32_e64 s[66:67], s0, v215
	v_bfe_u32 v224, v207, 10, 11
	v_add_u32_e32 v225, 0x800, v226
	v_lshl_add_u32 v222, v215, 2, v141
	v_add_u32_e32 v224, v225, v224
	s_andn2_b64 exec, exec, s[66:67]
	ds_write_b32 v222, v224
	s_mov_b64 exec, s[66:67]
	ds_write_b32 v227, v193
	s_mov_b64 exec, s[54:55]
	v_cmp_lt_u32_e64 s[66:67], s0, v216
	v_bfe_u32 v224, v208, 10, 11
	v_add_u32_e32 v225, 0x1000, v226
	v_lshl_add_u32 v222, v216, 2, v141
	v_add_u32_e32 v224, v225, v224
	s_andn2_b64 exec, exec, s[66:67]
	ds_write_b32 v222, v224
	s_mov_b64 exec, s[66:67]
	ds_write_b32 v227, v193
	s_mov_b64 exec, s[56:57]
	v_cmp_lt_u32_e64 s[66:67], s0, v217
	v_bfe_u32 v224, v209, 10, 11
	v_add_u32_e32 v225, 0x1800, v226
	v_lshl_add_u32 v222, v217, 2, v141
	v_add_u32_e32 v224, v225, v224
	s_andn2_b64 exec, exec, s[66:67]
	ds_write_b32 v222, v224
	s_mov_b64 exec, s[66:67]
	ds_write_b32 v227, v193
	s_waitcnt lgkmcnt(4)
	s_mov_b64 exec, s[58:59]
	v_cmp_lt_u32_e64 s[66:67], s0, v218
	v_bfe_u32 v224, v210, 10, 11
	v_add_u32_e32 v225, 0x8000, v226
	v_lshl_add_u32 v222, v218, 2, v141
	v_add_u32_e32 v224, v225, v224
	s_andn2_b64 exec, exec, s[66:67]
	ds_write_b32 v222, v224
	s_mov_b64 exec, s[66:67]
	ds_write_b32 v227, v193
	s_mov_b64 exec, s[60:61]
	v_cmp_lt_u32_e64 s[66:67], s0, v219
	v_bfe_u32 v224, v211, 10, 11
	v_add_u32_e32 v225, 0x8800, v226
	v_lshl_add_u32 v222, v219, 2, v141
	v_add_u32_e32 v224, v225, v224
	s_andn2_b64 exec, exec, s[66:67]
	ds_write_b32 v222, v224
	s_mov_b64 exec, s[66:67]
	ds_write_b32 v227, v193
	s_mov_b64 exec, s[62:63]
	v_cmp_lt_u32_e64 s[66:67], s0, v220
	v_bfe_u32 v224, v212, 10, 11
	v_add_u32_e32 v225, 0x9000, v226
	v_lshl_add_u32 v222, v220, 2, v141
	v_add_u32_e32 v224, v225, v224
	s_andn2_b64 exec, exec, s[66:67]
	ds_write_b32 v222, v224
	s_mov_b64 exec, s[66:67]
	ds_write_b32 v227, v193
	s_mov_b64 exec, s[64:65]
	v_cmp_lt_u32_e64 s[66:67], s0, v221
	v_bfe_u32 v224, v213, 10, 11
	v_add_u32_e32 v225, 0x9800, v226
	v_lshl_add_u32 v222, v221, 2, v141
	v_add_u32_e32 v224, v225, v224
	s_andn2_b64 exec, exec, s[66:67]
	ds_write_b32 v222, v224
	s_mov_b64 exec, s[66:67]
	ds_write_b32 v227, v193
	s_mov_b64 exec, s[14:15]
	v_mov_b32_e32 v104, v228
	v_lshlrev_b32_e32 v104, v143, v104
	ds_bpermute_b32 v105, v144, v104
	s_waitcnt lgkmcnt(0)
	v_or_b32_e32 v104, v105, v104
	ds_bpermute_b32 v105, v145, v104
	s_and_saveexec_b64 s[14:15], s[38:39]
	s_cbranch_execz .LBB0_1480
	s_waitcnt lgkmcnt(0)
	v_or_b32_e32 v106, v104, v105
	v_lshl_add_u64 v[104:105], v[122:123], 0, s[74:75]
	v_add_co_u32_e32 v104, vcc, 0x3f700000, v104
	s_nop 1
	v_addc_co_u32_e32 v105, vcc, 0, v105, vcc
	global_store_dword v[104:105], v106, off
.LBB0_1480:
	s_or_b64 exec, exec, s[14:15]
	s_add_i32 s31, s31, 16
	s_min_i32 s14, s31, s72
	v_lshl_or_b32 v104, s14, 5, v125
	s_waitcnt lgkmcnt(0)
	v_ashrrev_i32_e32 v105, 31, v104
	v_lshlrev_b64 v[104:105], 7, v[104:105]
	v_sub_u32_e32 v104, v104, v229
	v_lshl_add_u64 v[104:105], v[120:121], 0, v[104:105]
	global_load_dwordx4 v[116:119], v[104:105], off
	global_load_dwordx4 v[108:111], v[104:105], off offset:1024
	global_load_dwordx4 v[112:115], v[104:105], off offset:2048
	s_nop 0
	global_load_dwordx4 v[104:107], v[104:105], off offset:3072
	s_cmp_ge_i32 s85, s82
	s_cbranch_scc1 .LBB0_1437
	s_waitcnt vmcnt(7)
	v_mfma_f32_16x16x32_bf16 v[146:149], v[72:75], v[0:3], 0
	v_mfma_f32_16x16x32_bf16 v[178:181], v[72:75], v[244:247], 0
	s_waitcnt vmcnt(5)
	v_mfma_f32_16x16x32_bf16 v[150:153], v[80:83], v[0:3], 0
	v_mfma_f32_16x16x32_bf16 v[182:185], v[80:83], v[244:247], 0
	v_mfma_f32_16x16x32_bf16 v[154:157], v[76:79], v[4:7], v[146:149]
	v_mfma_f32_16x16x32_bf16 v[178:181], v[76:79], v[248:251], v[178:181]
	s_waitcnt vmcnt(4)
	v_mfma_f32_16x16x32_bf16 v[158:161], v[84:87], v[4:7], v[150:153]
	v_mfma_f32_16x16x32_bf16 v[182:185], v[84:87], v[248:251], v[182:185]
	v_mfma_f32_16x16x32_bf16 v[146:149], v[72:75], v[16:19], 0
	v_mfma_f32_16x16x32_bf16 v[150:153], v[80:83], v[16:19], 0
	v_mfma_f32_16x16x32_bf16 v[146:149], v[76:79], v[20:23], v[146:149]
	v_mfma_f32_16x16x32_bf16 v[150:153], v[84:87], v[20:23], v[150:153]
	s_nop 3
	v_fma_f32 v178, v12, |v154|, v178
	v_fma_f32 v182, v12, |v158|, v182
	v_fma_f32 v179, v12, |v155|, v179
	v_fma_f32 v183, v12, |v159|, v183
	v_fma_f32 v180, v12, |v156|, v180
	v_fma_f32 v184, v12, |v160|, v184
	v_fma_f32 v181, v12, |v157|, v181
	v_fma_f32 v185, v12, |v161|, v185
	v_mfma_f32_16x16x32_bf16 v[154:157], v[72:75], v[24:27], 0
	v_mfma_f32_16x16x32_bf16 v[158:161], v[80:83], v[24:27], 0
	v_mfma_f32_16x16x32_bf16 v[154:157], v[76:79], v[28:31], v[154:157]
	v_mfma_f32_16x16x32_bf16 v[158:161], v[84:87], v[28:31], v[158:161]
	s_nop 3
	v_fma_f32 v178, v13, |v146|, v178
	v_fma_f32 v182, v13, |v150|, v182
	v_fma_f32 v179, v13, |v147|, v179
	v_fma_f32 v183, v13, |v151|, v183
	v_fma_f32 v180, v13, |v148|, v180
	v_fma_f32 v184, v13, |v152|, v184
	v_fma_f32 v181, v13, |v149|, v181
	v_fma_f32 v185, v13, |v153|, v185
	v_mfma_f32_16x16x32_bf16 v[146:149], v[72:75], v[32:35], 0
	v_mfma_f32_16x16x32_bf16 v[150:153], v[80:83], v[32:35], 0
	v_mfma_f32_16x16x32_bf16 v[146:149], v[76:79], v[36:39], v[146:149]
	v_mfma_f32_16x16x32_bf16 v[150:153], v[84:87], v[36:39], v[150:153]
	s_nop 3
	v_fma_f32 v178, v14, |v154|, v178
	v_fma_f32 v182, v14, |v158|, v182
	v_fma_f32 v179, v14, |v155|, v179
	v_fma_f32 v183, v14, |v159|, v183
	v_fma_f32 v180, v14, |v156|, v180
	v_fma_f32 v184, v14, |v160|, v184
	v_fma_f32 v181, v14, |v157|, v181
	v_fma_f32 v185, v14, |v161|, v185
	v_mfma_f32_16x16x32_bf16 v[154:157], v[72:75], v[40:43], 0
	v_mfma_f32_16x16x32_bf16 v[158:161], v[80:83], v[40:43], 0
	v_mfma_f32_16x16x32_bf16 v[154:157], v[76:79], v[44:47], v[154:157]
	v_mfma_f32_16x16x32_bf16 v[158:161], v[84:87], v[44:47], v[158:161]
	s_nop 3
	v_fma_f32 v178, v15, |v146|, v178
	v_fma_f32 v182, v15, |v150|, v182
	v_fma_f32 v179, v15, |v147|, v179
	v_fma_f32 v183, v15, |v151|, v183
	v_fma_f32 v180, v15, |v148|, v180
	v_fma_f32 v184, v15, |v152|, v184
	v_fma_f32 v181, v15, |v149|, v181
	v_fma_f32 v185, v15, |v153|, v185
	v_mfma_f32_16x16x32_bf16 v[146:149], v[72:75], v[48:51], 0
	v_mfma_f32_16x16x32_bf16 v[150:153], v[80:83], v[48:51], 0
	v_mfma_f32_16x16x32_bf16 v[146:149], v[76:79], v[52:55], v[146:149]
	v_mfma_f32_16x16x32_bf16 v[150:153], v[84:87], v[52:55], v[150:153]
	s_nop 3
	v_fma_f32 v178, v8, |v154|, v178
	v_fma_f32 v182, v8, |v158|, v182
	v_fma_f32 v179, v8, |v155|, v179
	v_fma_f32 v183, v8, |v159|, v183
	v_fma_f32 v180, v8, |v156|, v180
	v_fma_f32 v184, v8, |v160|, v184
	v_fma_f32 v181, v8, |v157|, v181
	v_fma_f32 v185, v8, |v161|, v185
	v_mfma_f32_16x16x32_bf16 v[154:157], v[72:75], v[56:59], 0
	v_mfma_f32_16x16x32_bf16 v[158:161], v[80:83], v[56:59], 0
	v_mfma_f32_16x16x32_bf16 v[154:157], v[76:79], v[60:63], v[154:157]
	v_mfma_f32_16x16x32_bf16 v[158:161], v[84:87], v[60:63], v[158:161]
	s_nop 3
	v_fma_f32 v178, v9, |v146|, v178
	v_fma_f32 v182, v9, |v150|, v182
	v_fma_f32 v179, v9, |v147|, v179
	v_fma_f32 v183, v9, |v151|, v183
	v_fma_f32 v180, v9, |v148|, v180
	v_fma_f32 v184, v9, |v152|, v184
	v_fma_f32 v181, v9, |v149|, v181
	v_fma_f32 v185, v9, |v153|, v185
	v_mfma_f32_16x16x32_bf16 v[146:149], v[72:75], v[64:67], 0
	v_mfma_f32_16x16x32_bf16 v[150:153], v[80:83], v[64:67], 0
	v_mfma_f32_16x16x32_bf16 v[146:149], v[76:79], v[68:71], v[146:149]
	v_mfma_f32_16x16x32_bf16 v[150:153], v[84:87], v[68:71], v[150:153]
	s_nop 3
	v_fma_f32 v178, v10, |v154|, v178
	v_fma_f32 v182, v10, |v158|, v182
	v_fma_f32 v179, v10, |v155|, v179
	v_fma_f32 v183, v10, |v159|, v183
	v_fma_f32 v180, v10, |v156|, v180
	v_fma_f32 v184, v10, |v160|, v184
	v_fma_f32 v181, v10, |v157|, v181
	v_fma_f32 v185, v10, |v161|, v185
	s_nop 7
	v_fma_f32 v178, v11, |v146|, v178
	v_fma_f32 v182, v11, |v150|, v182
	v_fma_f32 v179, v11, |v147|, v179
	v_fma_f32 v183, v11, |v151|, v183
	v_fma_f32 v180, v11, |v148|, v180
	v_fma_f32 v184, v11, |v152|, v184
	v_fma_f32 v181, v11, |v149|, v181
	v_fma_f32 v185, v11, |v153|, v185
	v_cmp_ge_f32_e64 s[66:67], v178, v140
	v_cmp_ge_f32_e64 s[50:51], v178, v139
	v_cmp_ge_f32_e32 vcc, v179, v140
	v_cmp_ge_f32_e64 s[52:53], v179, v139
	v_cndmask_b32_e64 v224, 0, 1, s[66:67]
	v_cndmask_b32_e64 v225, 0, 2, vcc
	s_andn2_b64 s[50:51], s[50:51], s[66:67]
	s_andn2_b64 s[52:53], s[52:53], vcc
	v_or_b32_e32 v228, v224, v225
	v_cmp_ge_f32_e64 s[66:67], v180, v140
	v_cmp_ge_f32_e64 s[54:55], v180, v139
	v_cmp_ge_f32_e32 vcc, v181, v140
	v_cmp_ge_f32_e64 s[56:57], v181, v139
	v_cndmask_b32_e64 v224, 0, 4, s[66:67]
	v_cndmask_b32_e64 v225, 0, 8, vcc
	s_andn2_b64 s[54:55], s[54:55], s[66:67]
	s_andn2_b64 s[56:57], s[56:57], vcc
	v_or3_b32 v228, v228, v224, v225
	v_cmp_ge_f32_e64 s[66:67], v182, v140
	v_cmp_ge_f32_e64 s[58:59], v182, v139
	v_cmp_ge_f32_e32 vcc, v183, v140
	v_cmp_ge_f32_e64 s[60:61], v183, v139
	v_cndmask_b32_e64 v224, 0, v201, s[66:67]
	v_cndmask_b32_e64 v225, 0, v200, vcc
	s_andn2_b64 s[58:59], s[58:59], s[66:67]
	s_andn2_b64 s[60:61], s[60:61], vcc
	v_or3_b32 v228, v228, v224, v225
	v_cmp_ge_f32_e64 s[66:67], v184, v140
	v_cmp_ge_f32_e64 s[62:63], v184, v139
	v_cmp_ge_f32_e32 vcc, v185, v140
	v_cmp_ge_f32_e64 s[64:65], v185, v139
	v_cndmask_b32_e64 v224, 0, v199, s[66:67]
	v_cndmask_b32_e64 v225, 0, v198, vcc
	s_andn2_b64 s[62:63], s[62:63], s[66:67]
	s_andn2_b64 s[64:65], s[64:65], vcc
	v_or3_b32 v228, v228, v224, v225
	v_add_u32_e32 v226, s74, v124
	v_mov_b32_e32 v227, s96
	s_mov_b64 s[14:15], exec
	s_mov_b64 exec, s[50:51]
	v_ashrrev_i32_e32 v206, 31, v178
	v_xor_b32_e32 v206, v206, v178
	v_lshrrev_b32_e32 v222, 9, v206
	v_lshrrev_b32_e32 v223, 6, v206
	v_and_b32_e32 v222, 0xffc, v222
	v_and_b32_e32 v223, 16, v223
	v_add_u32_e32 v222, v128, v222
	v_lshlrev_b32_e64 v223, v223, 1
	ds_add_u32 v222, v223
	s_mov_b64 exec, s[52:53]
	v_ashrrev_i32_e32 v207, 31, v179
	v_xor_b32_e32 v207, v207, v179
	v_lshrrev_b32_e32 v222, 9, v207
	v_lshrrev_b32_e32 v223, 6, v207
	v_and_b32_e32 v222, 0xffc, v222
	v_and_b32_e32 v223, 16, v223
	v_add_u32_e32 v222, v128, v222
	v_lshlrev_b32_e64 v223, v223, 1
	ds_add_u32 v222, v223
	s_mov_b64 exec, s[54:55]
	v_ashrrev_i32_e32 v208, 31, v180
	v_xor_b32_e32 v208, v208, v180
	v_lshrrev_b32_e32 v222, 9, v208
	v_lshrrev_b32_e32 v223, 6, v208
	v_and_b32_e32 v222, 0xffc, v222
	v_and_b32_e32 v223, 16, v223
	v_add_u32_e32 v222, v128, v222
	v_lshlrev_b32_e64 v223, v223, 1
	ds_add_u32 v222, v223
	s_mov_b64 exec, s[56:57]
	v_ashrrev_i32_e32 v209, 31, v181
	v_xor_b32_e32 v209, v209, v181
	v_lshrrev_b32_e32 v222, 9, v209
	v_lshrrev_b32_e32 v223, 6, v209
	v_and_b32_e32 v222, 0xffc, v222
	v_and_b32_e32 v223, 16, v223
	v_add_u32_e32 v222, v128, v222
	v_lshlrev_b32_e64 v223, v223, 1
	ds_add_u32 v222, v223
	s_mov_b64 exec, s[58:59]
	v_ashrrev_i32_e32 v210, 31, v182
	v_xor_b32_e32 v210, v210, v182
	v_lshrrev_b32_e32 v222, 9, v210
	v_lshrrev_b32_e32 v223, 6, v210
	v_and_b32_e32 v222, 0xffc, v222
	v_and_b32_e32 v223, 16, v223
	v_add_u32_e32 v222, v128, v222
	v_lshlrev_b32_e64 v223, v223, 1
	ds_add_u32 v222, v223
	s_mov_b64 exec, s[60:61]
	v_ashrrev_i32_e32 v211, 31, v183
	v_xor_b32_e32 v211, v211, v183
	v_lshrrev_b32_e32 v222, 9, v211
	v_lshrrev_b32_e32 v223, 6, v211
	v_and_b32_e32 v222, 0xffc, v222
	v_and_b32_e32 v223, 16, v223
	v_add_u32_e32 v222, v128, v222
	v_lshlrev_b32_e64 v223, v223, 1
	ds_add_u32 v222, v223
	s_mov_b64 exec, s[62:63]
	v_ashrrev_i32_e32 v212, 31, v184
	v_xor_b32_e32 v212, v212, v184
	v_lshrrev_b32_e32 v222, 9, v212
	v_lshrrev_b32_e32 v223, 6, v212
	v_and_b32_e32 v222, 0xffc, v222
	v_and_b32_e32 v223, 16, v223
	v_add_u32_e32 v222, v128, v222
	v_lshlrev_b32_e64 v223, v223, 1
	ds_add_u32 v222, v223
	s_mov_b64 exec, s[64:65]
	v_ashrrev_i32_e32 v213, 31, v185
	v_xor_b32_e32 v213, v213, v185
	v_lshrrev_b32_e32 v222, 9, v213
	v_lshrrev_b32_e32 v223, 6, v213
	v_and_b32_e32 v222, 0xffc, v222
	v_and_b32_e32 v223, 16, v223
	v_add_u32_e32 v222, v128, v222
	v_lshlrev_b32_e64 v223, v223, 1
	ds_add_u32 v222, v223
	s_waitcnt lgkmcnt(6)
	s_mov_b64 exec, s[50:51]
	ds_add_rtn_u32 v214, v142, v193
	s_mov_b64 exec, s[52:53]
	ds_add_rtn_u32 v215, v142, v193
	s_mov_b64 exec, s[54:55]
	ds_add_rtn_u32 v216, v142, v193
	s_mov_b64 exec, s[56:57]
	ds_add_rtn_u32 v217, v142, v193
	s_mov_b64 exec, s[58:59]
	ds_add_rtn_u32 v218, v142, v193
	s_mov_b64 exec, s[60:61]
	ds_add_rtn_u32 v219, v142, v193
	s_mov_b64 exec, s[62:63]
	ds_add_rtn_u32 v220, v142, v193
	s_mov_b64 exec, s[64:65]
	ds_add_rtn_u32 v221, v142, v193
	s_waitcnt lgkmcnt(0)
	s_mov_b64 exec, s[50:51]
	v_cmp_lt_u32_e64 s[66:67], s0, v214
	v_bfe_u32 v224, v206, 10, 11
	v_add_u32_e32 v225, 0x80000, v226
	v_lshl_add_u32 v222, v214, 2, v141
	v_add_u32_e32 v224, v225, v224
	s_andn2_b64 exec, exec, s[66:67]
	ds_write_b32 v222, v224
	s_mov_b64 exec, s[66:67]
	ds_write_b32 v227, v193
	s_mov_b64 exec, s[52:53]
	v_cmp_lt_u32_e64 s[66:67], s0, v215
	v_bfe_u32 v224, v207, 10, 11
	v_add_u32_e32 v225, 0x80800, v226
	v_lshl_add_u32 v222, v215, 2, v141
	v_add_u32_e32 v224, v225, v224
	s_andn2_b64 exec, exec, s[66:67]
	ds_write_b32 v222, v224
	s_mov_b64 exec, s[66:67]
	ds_write_b32 v227, v193
	s_mov_b64 exec, s[54:55]
	v_cmp_lt_u32_e64 s[66:67], s0, v216
	v_bfe_u32 v224, v208, 10, 11
	v_add_u32_e32 v225, 0x81000, v226
	v_lshl_add_u32 v222, v216, 2, v141
	v_add_u32_e32 v224, v225, v224
	s_andn2_b64 exec, exec, s[66:67]
	ds_write_b32 v222, v224
	s_mov_b64 exec, s[66:67]
	ds_write_b32 v227, v193
	s_mov_b64 exec, s[56:57]
	v_cmp_lt_u32_e64 s[66:67], s0, v217
	v_bfe_u32 v224, v209, 10, 11
	v_add_u32_e32 v225, 0x81800, v226
	v_lshl_add_u32 v222, v217, 2, v141
	v_add_u32_e32 v224, v225, v224
	s_andn2_b64 exec, exec, s[66:67]
	ds_write_b32 v222, v224
	s_mov_b64 exec, s[66:67]
	ds_write_b32 v227, v193
	s_waitcnt lgkmcnt(4)
	s_mov_b64 exec, s[58:59]
	v_cmp_lt_u32_e64 s[66:67], s0, v218
	v_bfe_u32 v224, v210, 10, 11
	v_add_u32_e32 v225, 0x88000, v226
	v_lshl_add_u32 v222, v218, 2, v141
	v_add_u32_e32 v224, v225, v224
	s_andn2_b64 exec, exec, s[66:67]
	ds_write_b32 v222, v224
	s_mov_b64 exec, s[66:67]
	ds_write_b32 v227, v193
	s_mov_b64 exec, s[60:61]
	v_cmp_lt_u32_e64 s[66:67], s0, v219
	v_bfe_u32 v224, v211, 10, 11
	v_add_u32_e32 v225, 0x88800, v226
	v_lshl_add_u32 v222, v219, 2, v141
	v_add_u32_e32 v224, v225, v224
	s_andn2_b64 exec, exec, s[66:67]
	ds_write_b32 v222, v224
	s_mov_b64 exec, s[66:67]
	ds_write_b32 v227, v193
	s_mov_b64 exec, s[62:63]
	v_cmp_lt_u32_e64 s[66:67], s0, v220
	v_bfe_u32 v224, v212, 10, 11
	v_add_u32_e32 v225, 0x89000, v226
	v_lshl_add_u32 v222, v220, 2, v141
	v_add_u32_e32 v224, v225, v224
	s_andn2_b64 exec, exec, s[66:67]
	ds_write_b32 v222, v224
	s_mov_b64 exec, s[66:67]
	ds_write_b32 v227, v193
	s_mov_b64 exec, s[64:65]
	v_cmp_lt_u32_e64 s[66:67], s0, v221
	v_bfe_u32 v224, v213, 10, 11
	v_add_u32_e32 v225, 0x89800, v226
	v_lshl_add_u32 v222, v221, 2, v141
	v_add_u32_e32 v224, v225, v224
	s_andn2_b64 exec, exec, s[66:67]
	ds_write_b32 v222, v224
	s_mov_b64 exec, s[66:67]
	ds_write_b32 v227, v193
	s_mov_b64 exec, s[14:15]
	v_mov_b32_e32 v146, v228
	v_lshlrev_b32_e32 v146, v143, v146
	ds_bpermute_b32 v147, v144, v146
	s_waitcnt lgkmcnt(0)
	v_or_b32_e32 v146, v147, v146
	ds_bpermute_b32 v147, v145, v146
	s_and_saveexec_b64 s[14:15], s[38:39]
	s_cbranch_execz .LBB0_1436
	s_waitcnt lgkmcnt(0)
	v_or_b32_e32 v148, v146, v147
	v_lshl_add_u64 v[146:147], v[122:123], 0, s[74:75]
	v_add_co_u32_e32 v146, vcc, 0x3f780000, v146
	s_nop 1
	v_addc_co_u32_e32 v147, vcc, 0, v147, vcc
	global_store_dword v[146:147], v148, off
	s_branch .LBB0_1436

.LBB0_1533:
	v_mfma_f32_16x16x32_bf16 v[112:115], v[100:103], v[0:3], 0
	v_mfma_f32_16x16x32_bf16 v[156:159], v[100:103], v[244:247], 0
	v_mfma_f32_16x16x32_bf16 v[116:119], v[92:95], v[0:3], 0
	v_mfma_f32_16x16x32_bf16 v[160:163], v[92:95], v[244:247], 0
	v_mfma_f32_16x16x32_bf16 v[128:131], v[96:99], v[4:7], v[112:115]
	v_mfma_f32_16x16x32_bf16 v[156:159], v[96:99], v[248:251], v[156:159]
	v_mfma_f32_16x16x32_bf16 v[132:135], v[88:91], v[4:7], v[116:119]
	v_mfma_f32_16x16x32_bf16 v[160:163], v[88:91], v[248:251], v[160:163]
	v_mfma_f32_16x16x32_bf16 v[112:115], v[100:103], v[16:19], 0
	v_mfma_f32_16x16x32_bf16 v[116:119], v[92:95], v[16:19], 0
	v_mfma_f32_16x16x32_bf16 v[112:115], v[96:99], v[20:23], v[112:115]
	v_mfma_f32_16x16x32_bf16 v[116:119], v[88:91], v[20:23], v[116:119]
	s_nop 3
	v_fma_f32 v156, v12, |v128|, v156
	v_fma_f32 v160, v12, |v132|, v160
	v_fma_f32 v157, v12, |v129|, v157
	v_fma_f32 v161, v12, |v133|, v161
	v_fma_f32 v158, v12, |v130|, v158
	v_fma_f32 v162, v12, |v134|, v162
	v_fma_f32 v159, v12, |v131|, v159
	v_fma_f32 v163, v12, |v135|, v163
	v_mfma_f32_16x16x32_bf16 v[128:131], v[100:103], v[24:27], 0
	v_mfma_f32_16x16x32_bf16 v[132:135], v[92:95], v[24:27], 0
	v_mfma_f32_16x16x32_bf16 v[128:131], v[96:99], v[28:31], v[128:131]
	v_mfma_f32_16x16x32_bf16 v[132:135], v[88:91], v[28:31], v[132:135]
	s_nop 3
	v_fma_f32 v156, v13, |v112|, v156
	v_fma_f32 v160, v13, |v116|, v160
	v_fma_f32 v157, v13, |v113|, v157
	v_fma_f32 v161, v13, |v117|, v161
	v_fma_f32 v158, v13, |v114|, v158
	v_fma_f32 v162, v13, |v118|, v162
	v_fma_f32 v159, v13, |v115|, v159
	v_fma_f32 v163, v13, |v119|, v163
	v_mfma_f32_16x16x32_bf16 v[112:115], v[100:103], v[32:35], 0
	v_mfma_f32_16x16x32_bf16 v[116:119], v[92:95], v[32:35], 0
	v_mfma_f32_16x16x32_bf16 v[112:115], v[96:99], v[36:39], v[112:115]
	v_mfma_f32_16x16x32_bf16 v[116:119], v[88:91], v[36:39], v[116:119]
	s_nop 3
	v_fma_f32 v156, v14, |v128|, v156
	v_fma_f32 v160, v14, |v132|, v160
	v_fma_f32 v157, v14, |v129|, v157
	v_fma_f32 v161, v14, |v133|, v161
	v_fma_f32 v158, v14, |v130|, v158
	v_fma_f32 v162, v14, |v134|, v162
	v_fma_f32 v159, v14, |v131|, v159
	v_fma_f32 v163, v14, |v135|, v163
	v_mfma_f32_16x16x32_bf16 v[128:131], v[100:103], v[40:43], 0
	v_mfma_f32_16x16x32_bf16 v[132:135], v[92:95], v[40:43], 0
	v_mfma_f32_16x16x32_bf16 v[128:131], v[96:99], v[44:47], v[128:131]
	v_mfma_f32_16x16x32_bf16 v[132:135], v[88:91], v[44:47], v[132:135]
	s_nop 3
	v_fma_f32 v156, v15, |v112|, v156
	v_fma_f32 v160, v15, |v116|, v160
	v_fma_f32 v157, v15, |v113|, v157
	v_fma_f32 v161, v15, |v117|, v161
	v_fma_f32 v158, v15, |v114|, v158
	v_fma_f32 v162, v15, |v118|, v162
	v_fma_f32 v159, v15, |v115|, v159
	v_fma_f32 v163, v15, |v119|, v163
	v_mfma_f32_16x16x32_bf16 v[112:115], v[100:103], v[48:51], 0
	v_mfma_f32_16x16x32_bf16 v[116:119], v[92:95], v[48:51], 0
	v_mfma_f32_16x16x32_bf16 v[112:115], v[96:99], v[52:55], v[112:115]
	v_mfma_f32_16x16x32_bf16 v[116:119], v[88:91], v[52:55], v[116:119]
	s_nop 3
	v_fma_f32 v156, v8, |v128|, v156
	v_fma_f32 v160, v8, |v132|, v160
	v_fma_f32 v157, v8, |v129|, v157
	v_fma_f32 v161, v8, |v133|, v161
	v_fma_f32 v158, v8, |v130|, v158
	v_fma_f32 v162, v8, |v134|, v162
	v_fma_f32 v159, v8, |v131|, v159
	v_fma_f32 v163, v8, |v135|, v163
	v_mfma_f32_16x16x32_bf16 v[128:131], v[100:103], v[56:59], 0
	v_mfma_f32_16x16x32_bf16 v[132:135], v[92:95], v[56:59], 0
	v_mfma_f32_16x16x32_bf16 v[128:131], v[96:99], v[60:63], v[128:131]
	v_mfma_f32_16x16x32_bf16 v[132:135], v[88:91], v[60:63], v[132:135]
	s_nop 3
	v_fma_f32 v156, v9, |v112|, v156
	v_fma_f32 v160, v9, |v116|, v160
	v_fma_f32 v157, v9, |v113|, v157
	v_fma_f32 v161, v9, |v117|, v161
	v_fma_f32 v158, v9, |v114|, v158
	v_fma_f32 v162, v9, |v118|, v162
	v_fma_f32 v159, v9, |v115|, v159
	v_fma_f32 v163, v9, |v119|, v163
	v_mfma_f32_16x16x32_bf16 v[112:115], v[100:103], v[64:67], 0
	v_mfma_f32_16x16x32_bf16 v[116:119], v[92:95], v[64:67], 0
	v_mfma_f32_16x16x32_bf16 v[112:115], v[96:99], v[68:71], v[112:115]
	v_mfma_f32_16x16x32_bf16 v[116:119], v[88:91], v[68:71], v[116:119]
	s_nop 3
	v_fma_f32 v156, v10, |v128|, v156
	v_fma_f32 v160, v10, |v132|, v160
	v_fma_f32 v157, v10, |v129|, v157
	v_fma_f32 v161, v10, |v133|, v161
	v_fma_f32 v158, v10, |v130|, v158
	v_fma_f32 v162, v10, |v134|, v162
	v_fma_f32 v159, v10, |v131|, v159
	v_fma_f32 v163, v10, |v135|, v163
	s_nop 7
	v_fma_f32 v156, v11, |v112|, v156
	v_fma_f32 v160, v11, |v116|, v160
	v_fma_f32 v157, v11, |v113|, v157
	v_fma_f32 v161, v11, |v117|, v161
	v_fma_f32 v158, v11, |v114|, v158
	v_fma_f32 v162, v11, |v118|, v162
	v_fma_f32 v159, v11, |v115|, v159
	v_fma_f32 v163, v11, |v119|, v163
	v_ashrrev_i32_e32 v89, 31, v160
	v_ashrrev_i32_e32 v88, 31, v156
	v_bitop3_b32 v88, v88, v156, s12 bitop3:0x36
	v_lshrrev_b32_e32 v88, 10, v88
	v_bitop3_b32 v89, v89, v160, s12 bitop3:0x36
	v_ashrrev_i32_e32 v90, 31, v157
	s_waitcnt lgkmcnt(0)
	v_cmp_ge_u32_e32 vcc, v88, v108
	v_lshrrev_b32_e32 v89, 10, v89
	v_bitop3_b32 v90, v90, v157, s12 bitop3:0x36
	v_ashrrev_i32_e32 v91, 31, v161
	v_cndmask_b32_e64 v88, 0, 1, vcc
	v_cmp_lt_u32_e32 vcc, v89, v108
	v_lshrrev_b32_e32 v90, 10, v90
	v_bitop3_b32 v91, v91, v161, s12 bitop3:0x36
	v_ashrrev_i32_e32 v92, 31, v158
	v_cndmask_b32_e64 v89, v201, 0, vcc
	v_cmp_lt_u32_e32 vcc, v90, v108
	v_lshrrev_b32_e32 v91, 10, v91
	v_bitop3_b32 v92, v92, v158, s12 bitop3:0x36
	v_ashrrev_i32_e32 v93, 31, v162
	v_cndmask_b32_e64 v90, 2, 0, vcc
	v_cmp_lt_u32_e32 vcc, v91, v108
	v_lshrrev_b32_e32 v92, 10, v92
	v_bitop3_b32 v93, v93, v162, s12 bitop3:0x36
	v_ashrrev_i32_e32 v94, 31, v159
	v_cndmask_b32_e64 v91, v200, 0, vcc
	v_cmp_lt_u32_e32 vcc, v92, v108
	v_lshrrev_b32_e32 v93, 10, v93
	v_bitop3_b32 v94, v94, v159, s12 bitop3:0x36
	v_ashrrev_i32_e32 v95, 31, v163
	v_cndmask_b32_e64 v92, 4, 0, vcc
	v_cmp_lt_u32_e32 vcc, v93, v108
	v_lshrrev_b32_e32 v94, 10, v94
	v_bitop3_b32 v95, v95, v163, s12 bitop3:0x36
	v_cndmask_b32_e64 v93, v199, 0, vcc
	v_cmp_lt_u32_e32 vcc, v94, v108
	v_lshrrev_b32_e32 v95, 10, v95
	v_or3_b32 v88, v89, v88, v90
	v_cndmask_b32_e64 v94, 8, 0, vcc
	v_cmp_lt_u32_e32 vcc, v95, v108
	v_or3_b32 v88, v88, v91, v92
	s_nop 0
	v_cndmask_b32_e64 v95, v198, 0, vcc
	v_or_b32_e32 v94, v94, v95
	v_or3_b32 v88, v88, v93, v94
	v_lshlrev_b32_e32 v88, v109, v88
	ds_bpermute_b32 v89, v110, v88
	s_waitcnt lgkmcnt(0)
	v_or_b32_e32 v88, v88, v89
	ds_bpermute_b32 v89, v111, v88
	s_and_saveexec_b64 s[14:15], s[38:39]
	s_cbranch_execz .LBB0_1530
	s_waitcnt lgkmcnt(0)
	v_or_b32_e32 v88, v88, v89
	global_store_dword v[104:105], v88, off
	s_branch .LBB0_1530
